# baseline (speedup 1.0000x reference)
.Lmy_head_bar:
	s_barrier
.LBB1_3:
	s_waitcnt lgkmcnt(0)
	v_mfma_f32_32x32x16_f16 a[0:15], v[18:21], v[74:77], a[0:15]
	s_add_i32 s31, s30, 1
	s_cmp_lg_u32 s30, 2
	s_cselect_b32 s91, s31, 0
	s_mul_i32 s30, s30, 0x9000
	s_mul_i32 s92, s91, 0x9000
	s_add_i32 s96, s92, 0x9000
	s_cmp_lg_u32 s91, 2
	s_cselect_b32 s96, s96, 0
	s_add_i32 s96, s96, s93
	s_mov_b32 m0, s96
	v_add_u32_e32 v147, s30, v208
	global_load_lds_dwordx4 v164, s[94:95]
	s_add_u32 m0, s96, 0x1000
	v_add_u32_e32 v2, s30, v209
	global_load_lds_dwordx4 v165, s[94:95]
	s_add_u32 m0, s96, 0x2000
	v_add_u32_e32 v3, s30, v210
	global_load_lds_dwordx4 v166, s[94:95]
	s_add_u32 m0, s96, 0x3000
	v_add_u32_e32 v146, s92, v141
	global_load_lds_dwordx4 v167, s[94:95]
	s_add_u32 s30, s35, s20
	s_addc_u32 s31, s84, s21
	s_add_u32 m0, s96, 0x4000
	s_load_dwordx16 s[68:83], s[30:31], 0x80
	global_load_lds_dwordx4 v168, s[94:95]
	s_add_u32 m0, s96, 0x5000
	s_load_dwordx16 s[52:67], s[30:31], 0x8080
	global_load_lds_dwordx4 v169, s[94:95]
	s_add_u32 m0, s96, 0x6000
	ds_read_b128 v[90:93], v145
	global_load_lds_dwordx4 v170, s[94:95]
	s_add_u32 m0, s96, 0x7000
	ds_read_b128 v[82:85], v145 offset:2048
	global_load_lds_dwordx4 v171, s[94:95]
	v_mfma_f32_32x32x16_f16 a[240:255], v[38:41], v[74:77], a[240:255]
	ds_read_b128 v[50:53], v147
	v_pk_mul_f16 v148, v46, v136
	v_pk_mul_f16 v149, v42, v137
	v_pk_mul_f16 v150, v47, v136
	v_pk_mul_f16 v151, v43, v137
	v_mfma_f32_32x32x16_f16 a[16:31], v[18:21], v[126:129], a[16:31]
	ds_read_b128 v[54:57], v147 offset:4096
	v_pk_mul_f16 v152, v48, v136
	v_pk_mul_f16 v153, v44, v137
	v_pk_mul_f16 v154, v49, v136
	v_pk_mul_f16 v155, v45, v137
	v_mfma_f32_32x32x16_f16 a[224:239], v[38:41], v[126:129], a[224:239]
	ds_read_b128 v[58:61], v147 offset:8192
	v_pk_mul_f16 v156, v46, v140
	v_pk_mul_f16 v157, v42, v139
	v_pk_mul_f16 v158, v47, v140
	v_pk_mul_f16 v159, v43, v139
	v_mfma_f32_32x32x16_f16 a[32:47], v[18:21], v[122:125], a[32:47]
	ds_read_b128 v[62:65], v147 offset:12288
	v_pk_mul_f16 v160, v48, v140
	v_pk_mul_f16 v161, v44, v139
	v_pk_mul_f16 v162, v49, v140
	v_pk_mul_f16 v163, v45, v139
	v_mfma_f32_32x32x16_f16 a[208:223], v[38:41], v[122:125], a[208:223]
	ds_read_b128 v[66:69], v147 offset:16384
	v_pk_max_f16 v148, v148, v149
	v_pk_max_f16 v150, v150, v151
	v_pk_max_f16 v152, v152, v153
	v_pk_max_f16 v154, v154, v155
	v_mfma_f32_32x32x16_f16 a[48:63], v[18:21], v[118:121], a[48:63]
	ds_read_b128 v[70:73], v147 offset:20480
	v_pk_max_f16 v156, v156, v157
	v_pk_max_f16 v158, v158, v159
	v_pk_max_f16 v160, v160, v161
	v_pk_max_f16 v162, v162, v163
	v_mfma_f32_32x32x16_f16 a[192:207], v[38:41], v[118:121], a[192:207]
	ds_read_b128 v[78:81], v147 offset:24576
	v_cndmask_b32_e64 v114, v1, v148, s[36:37]
	s_mov_b64 vcc, s[38:39]
	v_cndmask_b32_sdwa v114, v1, v148, vcc dst_sel:WORD_1 dst_unused:UNUSED_PRESERVE src0_sel:WORD_1 src1_sel:WORD_1
	v_cndmask_b32_e64 v115, v1, v150, s[40:41]
	s_mov_b64 vcc, s[42:43]
	v_cndmask_b32_sdwa v115, v1, v150, vcc dst_sel:WORD_1 dst_unused:UNUSED_PRESERVE src0_sel:WORD_1 src1_sel:WORD_1
	v_mfma_f32_32x32x16_f16 a[64:79], v[18:21], v[106:109], a[64:79]
	ds_read_b128 v[102:105], v147 offset:28672
	v_cndmask_b32_e64 v116, v1, v152, s[44:45]
	s_mov_b64 vcc, s[46:47]
	v_cndmask_b32_sdwa v116, v1, v152, vcc dst_sel:WORD_1 dst_unused:UNUSED_PRESERVE src0_sel:WORD_1 src1_sel:WORD_1
	v_cndmask_b32_e64 v117, v1, v154, s[48:49]
	s_mov_b64 vcc, s[50:51]
	v_cndmask_b32_sdwa v117, v1, v154, vcc dst_sel:WORD_1 dst_unused:UNUSED_PRESERVE src0_sel:WORD_1 src1_sel:WORD_1
	v_mfma_f32_32x32x16_f16 a[176:191], v[38:41], v[106:109], a[176:191]
	v_cndmask_b32_e64 v110, v138, v156, s[4:5]
	s_mov_b64 vcc, s[6:7]
	v_cndmask_b32_sdwa v110, v138, v156, vcc dst_sel:WORD_1 dst_unused:UNUSED_PRESERVE src0_sel:WORD_1 src1_sel:WORD_1
	v_cndmask_b32_e64 v111, v138, v158, s[8:9]
	s_mov_b64 vcc, s[10:11]
	v_cndmask_b32_sdwa v111, v138, v158, vcc dst_sel:WORD_1 dst_unused:UNUSED_PRESERVE src0_sel:WORD_1 src1_sel:WORD_1
	v_mfma_f32_32x32x16_f16 a[112:127], v[18:21], v[98:101], a[112:127]
	v_cndmask_b32_e64 v112, v138, v160, s[12:13]
	s_mov_b64 vcc, s[14:15]
	v_cndmask_b32_sdwa v112, v138, v160, vcc dst_sel:WORD_1 dst_unused:UNUSED_PRESERVE src0_sel:WORD_1 src1_sel:WORD_1
	v_cndmask_b32_e64 v113, v138, v162, s[16:17]
	s_mov_b64 vcc, s[18:19]
	v_cndmask_b32_sdwa v113, v138, v162, vcc dst_sel:WORD_1 dst_unused:UNUSED_PRESERVE src0_sel:WORD_1 src1_sel:WORD_1
	v_mfma_f32_32x32x16_f16 a[160:175], v[38:41], v[98:101], a[160:175]
	v_pk_add_f16 v148, v115, v114
	v_pk_add_f16 v149, v116, v117
	v_mfma_f32_32x32x16_f16 a[128:143], v[18:21], v[94:97], a[128:143]
	v_pk_add_f16 v150, v111, v110
	v_pk_add_f16 v151, v112, v113
	v_mfma_f32_32x32x16_f16 a[144:159], v[38:41], v[94:97], a[144:159]
	v_pk_add_f16 v148, v148, v149
	v_pk_add_f16 v150, v150, v151
	v_mfma_f32_32x32x16_f16 a[80:95], v[18:21], v[86:89], a[80:95]
	v_fma_mix_f32 v134, v148, 1.0, v134 op_sel_hi:[1,0,0]
	v_fma_mix_f32 v135, v150, 1.0, v135 op_sel_hi:[1,0,0]
	v_mfma_f32_32x32x16_f16 a[96:111], v[38:41], v[86:89], a[96:111]
	v_fma_mix_f32 v134, v148, 1.0, v134 op_sel:[1,0,0] op_sel_hi:[1,0,0]
	v_fma_mix_f32 v135, v150, 1.0, v135 op_sel:[1,0,0] op_sel_hi:[1,0,0]
	s_waitcnt lgkmcnt(0)
	v_mfma_f32_32x32x16_f16 a[0:15], v[114:117], v[50:53], a[0:15]
	s_load_dwordx16 s[36:51], s[30:31], 0xc0
	s_load_dwordx16 s[4:19], s[30:31], 0x80c0
	ds_read_b128 v[46:49], v145 offset:32
	ds_read_b128 v[42:45], v145 offset:2080
	v_mfma_f32_32x32x16_f16 a[240:255], v[110:113], v[50:53], a[240:255]
	ds_read_b128 v[74:77], v2
	v_pk_mul_f16 v148, v90, v136
	v_pk_mul_f16 v149, v82, v137
	v_pk_mul_f16 v150, v91, v136
	v_pk_mul_f16 v151, v83, v137
	v_mfma_f32_32x32x16_f16 a[16:31], v[114:117], v[54:57], a[16:31]
	ds_read_b128 v[126:129], v2 offset:4096
	v_pk_mul_f16 v152, v92, v136
	v_pk_mul_f16 v153, v84, v137
	v_pk_mul_f16 v154, v93, v136
	v_pk_mul_f16 v155, v85, v137
	v_mfma_f32_32x32x16_f16 a[224:239], v[110:113], v[54:57], a[224:239]
	ds_read_b128 v[122:125], v2 offset:8192
	v_pk_mul_f16 v156, v90, v140
	v_pk_mul_f16 v157, v82, v139
	v_pk_mul_f16 v158, v91, v140
	v_pk_mul_f16 v159, v83, v139
	v_mfma_f32_32x32x16_f16 a[32:47], v[114:117], v[58:61], a[32:47]
	ds_read_b128 v[118:121], v2 offset:12288
	v_pk_mul_f16 v160, v92, v140
	v_pk_mul_f16 v161, v84, v139
	v_pk_mul_f16 v162, v93, v140
	v_pk_mul_f16 v163, v85, v139
	v_mfma_f32_32x32x16_f16 a[208:223], v[110:113], v[58:61], a[208:223]
	ds_read_b128 v[106:109], v2 offset:16384
	v_pk_max_f16 v148, v148, v149
	v_pk_max_f16 v150, v150, v151
	v_pk_max_f16 v152, v152, v153
	v_pk_max_f16 v154, v154, v155
	v_mfma_f32_32x32x16_f16 a[48:63], v[114:117], v[62:65], a[48:63]
	ds_read_b128 v[98:101], v2 offset:20480
	v_pk_max_f16 v156, v156, v157
	v_pk_max_f16 v158, v158, v159
	v_pk_max_f16 v160, v160, v161
	v_pk_max_f16 v162, v162, v163
	v_mfma_f32_32x32x16_f16 a[192:207], v[110:113], v[62:65], a[192:207]
	ds_read_b128 v[94:97], v2 offset:24576
	v_cndmask_b32_e64 v18, v1, v148, s[68:69]
	s_mov_b64 vcc, s[70:71]
	v_cndmask_b32_sdwa v18, v1, v148, vcc dst_sel:WORD_1 dst_unused:UNUSED_PRESERVE src0_sel:WORD_1 src1_sel:WORD_1
	v_cndmask_b32_e64 v19, v1, v150, s[72:73]
	s_mov_b64 vcc, s[74:75]
	v_cndmask_b32_sdwa v19, v1, v150, vcc dst_sel:WORD_1 dst_unused:UNUSED_PRESERVE src0_sel:WORD_1 src1_sel:WORD_1
	v_mfma_f32_32x32x16_f16 a[64:79], v[114:117], v[66:69], a[64:79]
	ds_read_b128 v[86:89], v2 offset:28672
	v_cndmask_b32_e64 v20, v1, v152, s[76:77]
	s_mov_b64 vcc, s[78:79]
	v_cndmask_b32_sdwa v20, v1, v152, vcc dst_sel:WORD_1 dst_unused:UNUSED_PRESERVE src0_sel:WORD_1 src1_sel:WORD_1
	v_cndmask_b32_e64 v21, v1, v154, s[80:81]
	s_mov_b64 vcc, s[82:83]
	v_cndmask_b32_sdwa v21, v1, v154, vcc dst_sel:WORD_1 dst_unused:UNUSED_PRESERVE src0_sel:WORD_1 src1_sel:WORD_1
	v_mfma_f32_32x32x16_f16 a[176:191], v[110:113], v[66:69], a[176:191]
	v_cndmask_b32_e64 v38, v138, v156, s[52:53]
	s_mov_b64 vcc, s[54:55]
	v_cndmask_b32_sdwa v38, v138, v156, vcc dst_sel:WORD_1 dst_unused:UNUSED_PRESERVE src0_sel:WORD_1 src1_sel:WORD_1
	v_cndmask_b32_e64 v39, v138, v158, s[56:57]
	s_mov_b64 vcc, s[58:59]
	v_cndmask_b32_sdwa v39, v138, v158, vcc dst_sel:WORD_1 dst_unused:UNUSED_PRESERVE src0_sel:WORD_1 src1_sel:WORD_1
	v_mfma_f32_32x32x16_f16 a[112:127], v[114:117], v[70:73], a[112:127]
	v_cndmask_b32_e64 v40, v138, v160, s[60:61]
	s_mov_b64 vcc, s[62:63]
	v_cndmask_b32_sdwa v40, v138, v160, vcc dst_sel:WORD_1 dst_unused:UNUSED_PRESERVE src0_sel:WORD_1 src1_sel:WORD_1
	v_cndmask_b32_e64 v41, v138, v162, s[64:65]
	s_mov_b64 vcc, s[66:67]
	v_cndmask_b32_sdwa v41, v138, v162, vcc dst_sel:WORD_1 dst_unused:UNUSED_PRESERVE src0_sel:WORD_1 src1_sel:WORD_1
	v_mfma_f32_32x32x16_f16 a[160:175], v[110:113], v[70:73], a[160:175]
	v_pk_add_f16 v148, v19, v18
	v_pk_add_f16 v149, v20, v21
	v_mfma_f32_32x32x16_f16 a[128:143], v[114:117], v[78:81], a[128:143]
	v_pk_add_f16 v150, v39, v38
	v_pk_add_f16 v151, v40, v41
	v_mfma_f32_32x32x16_f16 a[144:159], v[110:113], v[78:81], a[144:159]
	v_pk_add_f16 v148, v148, v149
	v_pk_add_f16 v150, v150, v151
	v_mfma_f32_32x32x16_f16 a[80:95], v[114:117], v[102:105], a[80:95]
	v_fma_mix_f32 v134, v148, 1.0, v134 op_sel_hi:[1,0,0]
	v_fma_mix_f32 v135, v150, 1.0, v135 op_sel_hi:[1,0,0]
	v_mfma_f32_32x32x16_f16 a[96:111], v[110:113], v[102:105], a[96:111]
	v_fma_mix_f32 v134, v148, 1.0, v134 op_sel:[1,0,0] op_sel_hi:[1,0,0]
	v_fma_mix_f32 v135, v150, 1.0, v135 op_sel:[1,0,0] op_sel_hi:[1,0,0]
	s_waitcnt lgkmcnt(0)
	v_mfma_f32_32x32x16_f16 a[0:15], v[18:21], v[74:77], a[0:15]
	s_load_dwordx16 s[68:83], s[30:31], 0x100
	s_load_dwordx16 s[52:67], s[30:31], 0x8100
	ds_read_b128 v[90:93], v145 offset:64
	ds_read_b128 v[82:85], v145 offset:2112
	v_mfma_f32_32x32x16_f16 a[240:255], v[38:41], v[74:77], a[240:255]
	ds_read_b128 v[50:53], v3
	v_pk_mul_f16 v148, v46, v136
	v_pk_mul_f16 v149, v42, v137
	v_pk_mul_f16 v150, v47, v136
	v_pk_mul_f16 v151, v43, v137
	v_mfma_f32_32x32x16_f16 a[16:31], v[18:21], v[126:129], a[16:31]
	ds_read_b128 v[54:57], v3 offset:4096
	v_pk_mul_f16 v152, v48, v136
	v_pk_mul_f16 v153, v44, v137
	v_pk_mul_f16 v154, v49, v136
	v_pk_mul_f16 v155, v45, v137
	v_mfma_f32_32x32x16_f16 a[224:239], v[38:41], v[126:129], a[224:239]
	ds_read_b128 v[58:61], v3 offset:8192
	v_pk_mul_f16 v156, v46, v140
	v_pk_mul_f16 v157, v42, v139
	v_pk_mul_f16 v158, v47, v140
	v_pk_mul_f16 v159, v43, v139
	v_mfma_f32_32x32x16_f16 a[32:47], v[18:21], v[122:125], a[32:47]
	ds_read_b128 v[62:65], v3 offset:12288
	v_pk_mul_f16 v160, v48, v140
	v_pk_mul_f16 v161, v44, v139
	v_pk_mul_f16 v162, v49, v140
	v_pk_mul_f16 v163, v45, v139
	v_mfma_f32_32x32x16_f16 a[208:223], v[38:41], v[122:125], a[208:223]
	ds_read_b128 v[66:69], v3 offset:16384
	v_pk_max_f16 v148, v148, v149
	v_pk_max_f16 v150, v150, v151
	v_pk_max_f16 v152, v152, v153
	v_pk_max_f16 v154, v154, v155
	v_mfma_f32_32x32x16_f16 a[48:63], v[18:21], v[118:121], a[48:63]
	ds_read_b128 v[70:73], v3 offset:20480
	v_pk_max_f16 v156, v156, v157
	v_pk_max_f16 v158, v158, v159
	v_pk_max_f16 v160, v160, v161
	v_pk_max_f16 v162, v162, v163
	v_mfma_f32_32x32x16_f16 a[192:207], v[38:41], v[118:121], a[192:207]
	ds_read_b128 v[78:81], v3 offset:24576
	v_cndmask_b32_e64 v114, v1, v148, s[36:37]
	s_mov_b64 vcc, s[38:39]
	v_cndmask_b32_sdwa v114, v1, v148, vcc dst_sel:WORD_1 dst_unused:UNUSED_PRESERVE src0_sel:WORD_1 src1_sel:WORD_1
	v_cndmask_b32_e64 v115, v1, v150, s[40:41]
	s_mov_b64 vcc, s[42:43]
	v_cndmask_b32_sdwa v115, v1, v150, vcc dst_sel:WORD_1 dst_unused:UNUSED_PRESERVE src0_sel:WORD_1 src1_sel:WORD_1
	v_mfma_f32_32x32x16_f16 a[64:79], v[18:21], v[106:109], a[64:79]
	ds_read_b128 v[102:105], v3 offset:28672
	v_cndmask_b32_e64 v116, v1, v152, s[44:45]
	s_mov_b64 vcc, s[46:47]
	v_cndmask_b32_sdwa v116, v1, v152, vcc dst_sel:WORD_1 dst_unused:UNUSED_PRESERVE src0_sel:WORD_1 src1_sel:WORD_1
	v_cndmask_b32_e64 v117, v1, v154, s[48:49]
	s_mov_b64 vcc, s[50:51]
	v_cndmask_b32_sdwa v117, v1, v154, vcc dst_sel:WORD_1 dst_unused:UNUSED_PRESERVE src0_sel:WORD_1 src1_sel:WORD_1
	v_mfma_f32_32x32x16_f16 a[176:191], v[38:41], v[106:109], a[176:191]
	v_cndmask_b32_e64 v110, v138, v156, s[4:5]
	s_mov_b64 vcc, s[6:7]
	v_cndmask_b32_sdwa v110, v138, v156, vcc dst_sel:WORD_1 dst_unused:UNUSED_PRESERVE src0_sel:WORD_1 src1_sel:WORD_1
	v_cndmask_b32_e64 v111, v138, v158, s[8:9]
	s_mov_b64 vcc, s[10:11]
	v_cndmask_b32_sdwa v111, v138, v158, vcc dst_sel:WORD_1 dst_unused:UNUSED_PRESERVE src0_sel:WORD_1 src1_sel:WORD_1
	v_mfma_f32_32x32x16_f16 a[112:127], v[18:21], v[98:101], a[112:127]
	v_cndmask_b32_e64 v112, v138, v160, s[12:13]
	s_mov_b64 vcc, s[14:15]
	v_cndmask_b32_sdwa v112, v138, v160, vcc dst_sel:WORD_1 dst_unused:UNUSED_PRESERVE src0_sel:WORD_1 src1_sel:WORD_1
	v_cndmask_b32_e64 v113, v138, v162, s[16:17]
	s_mov_b64 vcc, s[18:19]
	v_cndmask_b32_sdwa v113, v138, v162, vcc dst_sel:WORD_1 dst_unused:UNUSED_PRESERVE src0_sel:WORD_1 src1_sel:WORD_1
	v_mfma_f32_32x32x16_f16 a[160:175], v[38:41], v[98:101], a[160:175]
	v_pk_add_f16 v148, v115, v114
	v_pk_add_f16 v149, v116, v117
	v_mfma_f32_32x32x16_f16 a[128:143], v[18:21], v[94:97], a[128:143]
	v_pk_add_f16 v150, v111, v110
	v_pk_add_f16 v151, v112, v113
	v_mfma_f32_32x32x16_f16 a[144:159], v[38:41], v[94:97], a[144:159]
	v_pk_add_f16 v148, v148, v149
	v_pk_add_f16 v150, v150, v151
	v_mfma_f32_32x32x16_f16 a[80:95], v[18:21], v[86:89], a[80:95]
	v_fma_mix_f32 v134, v148, 1.0, v134 op_sel_hi:[1,0,0]
	v_fma_mix_f32 v135, v150, 1.0, v135 op_sel_hi:[1,0,0]
	v_mfma_f32_32x32x16_f16 a[96:111], v[38:41], v[86:89], a[96:111]
	v_fma_mix_f32 v134, v148, 1.0, v134 op_sel:[1,0,0] op_sel_hi:[1,0,0]
	v_fma_mix_f32 v135, v150, 1.0, v135 op_sel:[1,0,0] op_sel_hi:[1,0,0]
	s_waitcnt lgkmcnt(0)
	v_mfma_f32_32x32x16_f16 a[0:15], v[114:117], v[50:53], a[0:15]
	s_load_dwordx16 s[36:51], s[30:31], 0x140
	s_load_dwordx16 s[4:19], s[30:31], 0x8140
	ds_read_b128 v[46:49], v145 offset:96
	ds_read_b128 v[42:45], v145 offset:2144
	v_mfma_f32_32x32x16_f16 a[240:255], v[110:113], v[50:53], a[240:255]
	ds_read_b128 v[74:77], v146
	v_pk_mul_f16 v148, v90, v136
	v_pk_mul_f16 v149, v82, v137
	v_pk_mul_f16 v150, v91, v136
	v_pk_mul_f16 v151, v83, v137
	v_mfma_f32_32x32x16_f16 a[16:31], v[114:117], v[54:57], a[16:31]
	ds_read_b128 v[126:129], v146 offset:4096
	v_pk_mul_f16 v152, v92, v136
	v_pk_mul_f16 v153, v84, v137
	v_pk_mul_f16 v154, v93, v136
	v_pk_mul_f16 v155, v85, v137
	v_mfma_f32_32x32x16_f16 a[224:239], v[110:113], v[54:57], a[224:239]
	ds_read_b128 v[122:125], v146 offset:8192
	v_pk_mul_f16 v156, v90, v140
	v_pk_mul_f16 v157, v82, v139
	v_pk_mul_f16 v158, v91, v140
	v_pk_mul_f16 v159, v83, v139
	v_mfma_f32_32x32x16_f16 a[32:47], v[114:117], v[58:61], a[32:47]
	ds_read_b128 v[118:121], v146 offset:12288
	v_pk_mul_f16 v160, v92, v140
	v_pk_mul_f16 v161, v84, v139
	v_pk_mul_f16 v162, v93, v140
	v_pk_mul_f16 v163, v85, v139
	v_mfma_f32_32x32x16_f16 a[208:223], v[110:113], v[58:61], a[208:223]
	ds_read_b128 v[106:109], v146 offset:16384
	v_pk_max_f16 v148, v148, v149
	v_pk_max_f16 v150, v150, v151
	v_pk_max_f16 v152, v152, v153
	v_pk_max_f16 v154, v154, v155
	v_mfma_f32_32x32x16_f16 a[48:63], v[114:117], v[62:65], a[48:63]
	ds_read_b128 v[98:101], v146 offset:20480
	v_pk_max_f16 v156, v156, v157
	v_pk_max_f16 v158, v158, v159
	v_pk_max_f16 v160, v160, v161
	v_pk_max_f16 v162, v162, v163
	v_mfma_f32_32x32x16_f16 a[192:207], v[110:113], v[62:65], a[192:207]
	ds_read_b128 v[94:97], v146 offset:24576
	v_cndmask_b32_e64 v18, v1, v148, s[68:69]
	s_mov_b64 vcc, s[70:71]
	v_cndmask_b32_sdwa v18, v1, v148, vcc dst_sel:WORD_1 dst_unused:UNUSED_PRESERVE src0_sel:WORD_1 src1_sel:WORD_1
	v_cndmask_b32_e64 v19, v1, v150, s[72:73]
	s_mov_b64 vcc, s[74:75]
	v_cndmask_b32_sdwa v19, v1, v150, vcc dst_sel:WORD_1 dst_unused:UNUSED_PRESERVE src0_sel:WORD_1 src1_sel:WORD_1
	v_mfma_f32_32x32x16_f16 a[64:79], v[114:117], v[66:69], a[64:79]
	ds_read_b128 v[86:89], v146 offset:28672
	v_cndmask_b32_e64 v20, v1, v152, s[76:77]
	s_mov_b64 vcc, s[78:79]
	v_cndmask_b32_sdwa v20, v1, v152, vcc dst_sel:WORD_1 dst_unused:UNUSED_PRESERVE src0_sel:WORD_1 src1_sel:WORD_1
	v_cndmask_b32_e64 v21, v1, v154, s[80:81]
	s_mov_b64 vcc, s[82:83]
	v_cndmask_b32_sdwa v21, v1, v154, vcc dst_sel:WORD_1 dst_unused:UNUSED_PRESERVE src0_sel:WORD_1 src1_sel:WORD_1
	v_mfma_f32_32x32x16_f16 a[176:191], v[110:113], v[66:69], a[176:191]
	v_cndmask_b32_e64 v38, v138, v156, s[52:53]
	s_mov_b64 vcc, s[54:55]
	v_cndmask_b32_sdwa v38, v138, v156, vcc dst_sel:WORD_1 dst_unused:UNUSED_PRESERVE src0_sel:WORD_1 src1_sel:WORD_1
	v_cndmask_b32_e64 v39, v138, v158, s[56:57]
	s_mov_b64 vcc, s[58:59]
	v_cndmask_b32_sdwa v39, v138, v158, vcc dst_sel:WORD_1 dst_unused:UNUSED_PRESERVE src0_sel:WORD_1 src1_sel:WORD_1
	v_mfma_f32_32x32x16_f16 a[112:127], v[114:117], v[70:73], a[112:127]
	v_cndmask_b32_e64 v40, v138, v160, s[60:61]
	s_mov_b64 vcc, s[62:63]
	v_cndmask_b32_sdwa v40, v138, v160, vcc dst_sel:WORD_1 dst_unused:UNUSED_PRESERVE src0_sel:WORD_1 src1_sel:WORD_1
	v_cndmask_b32_e64 v41, v138, v162, s[64:65]
	s_mov_b64 vcc, s[66:67]
	v_cndmask_b32_sdwa v41, v138, v162, vcc dst_sel:WORD_1 dst_unused:UNUSED_PRESERVE src0_sel:WORD_1 src1_sel:WORD_1
	v_mfma_f32_32x32x16_f16 a[160:175], v[110:113], v[70:73], a[160:175]
	v_pk_add_f16 v148, v19, v18
	v_pk_add_f16 v149, v20, v21
	v_mfma_f32_32x32x16_f16 a[128:143], v[114:117], v[78:81], a[128:143]
	v_pk_add_f16 v150, v39, v38
	v_pk_add_f16 v151, v40, v41
	v_mfma_f32_32x32x16_f16 a[144:159], v[110:113], v[78:81], a[144:159]
	v_pk_add_f16 v148, v148, v149
	v_pk_add_f16 v150, v150, v151
	v_mfma_f32_32x32x16_f16 a[80:95], v[114:117], v[102:105], a[80:95]
	v_fma_mix_f32 v134, v148, 1.0, v134 op_sel_hi:[1,0,0]
	v_fma_mix_f32 v135, v150, 1.0, v135 op_sel_hi:[1,0,0]
	v_mfma_f32_32x32x16_f16 a[96:111], v[110:113], v[102:105], a[96:111]
	v_fma_mix_f32 v134, v148, 1.0, v134 op_sel:[1,0,0] op_sel_hi:[1,0,0]
	v_fma_mix_f32 v135, v150, 1.0, v135 op_sel:[1,0,0] op_sel_hi:[1,0,0]
	s_add_i32 s92, s92, 0x9000
	s_cmp_lg_u32 s91, 2
	s_cselect_b32 s30, s92, 0
	s_add_u32 s20, s20, 0x100
	s_addc_u32 s21, s21, 0
	s_add_u32 s94, s94, 0x8000
	s_addc_u32 s95, s95, 0
	v_add_u32_e32 v145, 0x80, v145
	s_cmpk_eq_i32 s20, 0xf00
	s_mov_b32 s30, s91
	s_waitcnt vmcnt(0)
	s_waitcnt lgkmcnt(0)
	s_cbranch_scc0 .Lmy_head_bar
	s_barrier
	s_waitcnt lgkmcnt(0)
	v_mfma_f32_32x32x16_f16 a[0:15], v[18:21], v[74:77], a[0:15]
	s_load_dwordx16 s[68:83], s[0:1], 0xf80
	s_load_dwordx16 s[52:67], s[0:1], 0x8f80
	ds_read_b128 v[90:93], v142 offset:1984
	ds_read_b128 v[82:85], v142 offset:4032
	v_mfma_f32_32x32x16_f16 a[240:255], v[38:41], v[74:77], a[240:255]
	ds_read_b128 v[50:53], v208
	v_pk_mul_f16 v148, v46, v136
	v_pk_mul_f16 v149, v42, v137
	v_pk_mul_f16 v150, v47, v136
	v_pk_mul_f16 v151, v43, v137
	v_mfma_f32_32x32x16_f16 a[16:31], v[18:21], v[126:129], a[16:31]
	ds_read_b128 v[54:57], v208 offset:4096
	v_pk_mul_f16 v152, v48, v136
	v_pk_mul_f16 v153, v44, v137
	v_pk_mul_f16 v154, v49, v136
	v_pk_mul_f16 v155, v45, v137
	v_mfma_f32_32x32x16_f16 a[224:239], v[38:41], v[126:129], a[224:239]
	ds_read_b128 v[58:61], v208 offset:8192
	v_pk_mul_f16 v156, v46, v140
	v_pk_mul_f16 v157, v42, v139
	v_pk_mul_f16 v158, v47, v140
	v_pk_mul_f16 v159, v43, v139
	v_mfma_f32_32x32x16_f16 a[32:47], v[18:21], v[122:125], a[32:47]
	ds_read_b128 v[62:65], v208 offset:12288
	v_pk_mul_f16 v160, v48, v140
	v_pk_mul_f16 v161, v44, v139
	v_pk_mul_f16 v162, v49, v140
	v_pk_mul_f16 v163, v45, v139
	v_mfma_f32_32x32x16_f16 a[208:223], v[38:41], v[122:125], a[208:223]
	ds_read_b128 v[66:69], v208 offset:16384
	v_pk_max_f16 v148, v148, v149
	v_pk_max_f16 v150, v150, v151
	v_pk_max_f16 v152, v152, v153
	v_pk_max_f16 v154, v154, v155
	v_mfma_f32_32x32x16_f16 a[48:63], v[18:21], v[118:121], a[48:63]
	ds_read_b128 v[70:73], v208 offset:20480
	v_pk_max_f16 v156, v156, v157
	v_pk_max_f16 v158, v158, v159
	v_pk_max_f16 v160, v160, v161
	v_pk_max_f16 v162, v162, v163
	v_mfma_f32_32x32x16_f16 a[192:207], v[38:41], v[118:121], a[192:207]
	ds_read_b128 v[78:81], v208 offset:24576
	v_cndmask_b32_e64 v114, v1, v148, s[36:37]
	s_mov_b64 vcc, s[38:39]
	v_cndmask_b32_sdwa v114, v1, v148, vcc dst_sel:WORD_1 dst_unused:UNUSED_PRESERVE src0_sel:WORD_1 src1_sel:WORD_1
	v_cndmask_b32_e64 v115, v1, v150, s[40:41]
	s_mov_b64 vcc, s[42:43]
	v_cndmask_b32_sdwa v115, v1, v150, vcc dst_sel:WORD_1 dst_unused:UNUSED_PRESERVE src0_sel:WORD_1 src1_sel:WORD_1
	v_mfma_f32_32x32x16_f16 a[64:79], v[18:21], v[106:109], a[64:79]
	ds_read_b128 v[102:105], v208 offset:28672
	v_cndmask_b32_e64 v116, v1, v152, s[44:45]
	s_mov_b64 vcc, s[46:47]
	v_cndmask_b32_sdwa v116, v1, v152, vcc dst_sel:WORD_1 dst_unused:UNUSED_PRESERVE src0_sel:WORD_1 src1_sel:WORD_1
	v_cndmask_b32_e64 v117, v1, v154, s[48:49]
	s_mov_b64 vcc, s[50:51]
	v_cndmask_b32_sdwa v117, v1, v154, vcc dst_sel:WORD_1 dst_unused:UNUSED_PRESERVE src0_sel:WORD_1 src1_sel:WORD_1
	v_mfma_f32_32x32x16_f16 a[176:191], v[38:41], v[106:109], a[176:191]
	v_cndmask_b32_e64 v110, v138, v156, s[4:5]
	s_mov_b64 vcc, s[6:7]
	v_cndmask_b32_sdwa v110, v138, v156, vcc dst_sel:WORD_1 dst_unused:UNUSED_PRESERVE src0_sel:WORD_1 src1_sel:WORD_1
	v_cndmask_b32_e64 v111, v138, v158, s[8:9]
	s_mov_b64 vcc, s[10:11]
	v_cndmask_b32_sdwa v111, v138, v158, vcc dst_sel:WORD_1 dst_unused:UNUSED_PRESERVE src0_sel:WORD_1 src1_sel:WORD_1
	v_mfma_f32_32x32x16_f16 a[112:127], v[18:21], v[98:101], a[112:127]
	v_cndmask_b32_e64 v112, v138, v160, s[12:13]
	s_mov_b64 vcc, s[14:15]
	v_cndmask_b32_sdwa v112, v138, v160, vcc dst_sel:WORD_1 dst_unused:UNUSED_PRESERVE src0_sel:WORD_1 src1_sel:WORD_1
	v_cndmask_b32_e64 v113, v138, v162, s[16:17]
	s_mov_b64 vcc, s[18:19]
	v_cndmask_b32_sdwa v113, v138, v162, vcc dst_sel:WORD_1 dst_unused:UNUSED_PRESERVE src0_sel:WORD_1 src1_sel:WORD_1
	v_mfma_f32_32x32x16_f16 a[160:175], v[38:41], v[98:101], a[160:175]
	v_pk_add_f16 v148, v115, v114
	v_pk_add_f16 v149, v116, v117
	v_mfma_f32_32x32x16_f16 a[128:143], v[18:21], v[94:97], a[128:143]
	v_pk_add_f16 v150, v111, v110
	v_pk_add_f16 v151, v112, v113
	v_mfma_f32_32x32x16_f16 a[144:159], v[38:41], v[94:97], a[144:159]
	v_pk_add_f16 v148, v148, v149
	v_pk_add_f16 v150, v150, v151
	v_mfma_f32_32x32x16_f16 a[80:95], v[18:21], v[86:89], a[80:95]
	v_fma_mix_f32 v134, v148, 1.0, v134 op_sel_hi:[1,0,0]
	v_fma_mix_f32 v135, v150, 1.0, v135 op_sel_hi:[1,0,0]
	v_mfma_f32_32x32x16_f16 a[96:111], v[38:41], v[86:89], a[96:111]
	v_fma_mix_f32 v134, v148, 1.0, v134 op_sel:[1,0,0] op_sel_hi:[1,0,0]
	v_fma_mix_f32 v135, v150, 1.0, v135 op_sel:[1,0,0] op_sel_hi:[1,0,0]
	s_waitcnt lgkmcnt(0)
	v_mfma_f32_32x32x16_f16 a[0:15], v[114:117], v[50:53], a[0:15]
	s_load_dwordx16 s[36:51], s[0:1], 0xfc0
	s_load_dwordx16 s[4:19], s[0:1], 0x8fc0
	ds_read_b128 v[46:49], v142 offset:2016
	ds_read_b128 v[42:45], v142 offset:4064
	v_mfma_f32_32x32x16_f16 a[240:255], v[110:113], v[50:53], a[240:255]
	ds_read_b128 v[74:77], v209
	v_pk_mul_f16 v148, v90, v136
	v_pk_mul_f16 v149, v82, v137
	v_pk_mul_f16 v150, v91, v136
	v_pk_mul_f16 v151, v83, v137
	v_mfma_f32_32x32x16_f16 a[16:31], v[114:117], v[54:57], a[16:31]
	ds_read_b128 v[126:129], v209 offset:4096
	v_pk_mul_f16 v152, v92, v136
	v_pk_mul_f16 v153, v84, v137
	v_pk_mul_f16 v154, v93, v136
	v_pk_mul_f16 v155, v85, v137
	v_mfma_f32_32x32x16_f16 a[224:239], v[110:113], v[54:57], a[224:239]
	ds_read_b128 v[122:125], v209 offset:8192
	v_pk_mul_f16 v156, v90, v140
	v_pk_mul_f16 v157, v82, v139
	v_pk_mul_f16 v158, v91, v140
	v_pk_mul_f16 v159, v83, v139
	v_mfma_f32_32x32x16_f16 a[32:47], v[114:117], v[58:61], a[32:47]
	ds_read_b128 v[118:121], v209 offset:12288
	v_pk_mul_f16 v160, v92, v140
	v_pk_mul_f16 v161, v84, v139
	v_pk_mul_f16 v162, v93, v140
	v_pk_mul_f16 v163, v85, v139
	v_mfma_f32_32x32x16_f16 a[208:223], v[110:113], v[58:61], a[208:223]
	ds_read_b128 v[106:109], v209 offset:16384
	v_pk_max_f16 v148, v148, v149
	v_pk_max_f16 v150, v150, v151
	v_pk_max_f16 v152, v152, v153
	v_pk_max_f16 v154, v154, v155
	v_mfma_f32_32x32x16_f16 a[48:63], v[114:117], v[62:65], a[48:63]
	ds_read_b128 v[98:101], v209 offset:20480
	v_pk_max_f16 v156, v156, v157
	v_pk_max_f16 v158, v158, v159
	v_pk_max_f16 v160, v160, v161
	v_pk_max_f16 v162, v162, v163
	v_mfma_f32_32x32x16_f16 a[192:207], v[110:113], v[62:65], a[192:207]
	ds_read_b128 v[94:97], v209 offset:24576
	v_cndmask_b32_e64 v18, v1, v148, s[68:69]
	s_mov_b64 vcc, s[70:71]
	v_cndmask_b32_sdwa v18, v1, v148, vcc dst_sel:WORD_1 dst_unused:UNUSED_PRESERVE src0_sel:WORD_1 src1_sel:WORD_1
	v_cndmask_b32_e64 v19, v1, v150, s[72:73]
	s_mov_b64 vcc, s[74:75]
	v_cndmask_b32_sdwa v19, v1, v150, vcc dst_sel:WORD_1 dst_unused:UNUSED_PRESERVE src0_sel:WORD_1 src1_sel:WORD_1
	v_mfma_f32_32x32x16_f16 a[64:79], v[114:117], v[66:69], a[64:79]
	ds_read_b128 v[86:89], v209 offset:28672
	v_cndmask_b32_e64 v20, v1, v152, s[76:77]
	s_mov_b64 vcc, s[78:79]
	v_cndmask_b32_sdwa v20, v1, v152, vcc dst_sel:WORD_1 dst_unused:UNUSED_PRESERVE src0_sel:WORD_1 src1_sel:WORD_1
	v_cndmask_b32_e64 v21, v1, v154, s[80:81]
	s_mov_b64 vcc, s[82:83]
	v_cndmask_b32_sdwa v21, v1, v154, vcc dst_sel:WORD_1 dst_unused:UNUSED_PRESERVE src0_sel:WORD_1 src1_sel:WORD_1
	v_mfma_f32_32x32x16_f16 a[176:191], v[110:113], v[66:69], a[176:191]
	v_cndmask_b32_e64 v38, v138, v156, s[52:53]
	s_mov_b64 vcc, s[54:55]
	v_cndmask_b32_sdwa v38, v138, v156, vcc dst_sel:WORD_1 dst_unused:UNUSED_PRESERVE src0_sel:WORD_1 src1_sel:WORD_1
	v_cndmask_b32_e64 v39, v138, v158, s[56:57]
	s_mov_b64 vcc, s[58:59]
	v_cndmask_b32_sdwa v39, v138, v158, vcc dst_sel:WORD_1 dst_unused:UNUSED_PRESERVE src0_sel:WORD_1 src1_sel:WORD_1
	v_mfma_f32_32x32x16_f16 a[112:127], v[114:117], v[70:73], a[112:127]
	v_cndmask_b32_e64 v40, v138, v160, s[60:61]
	s_mov_b64 vcc, s[62:63]
	v_cndmask_b32_sdwa v40, v138, v160, vcc dst_sel:WORD_1 dst_unused:UNUSED_PRESERVE src0_sel:WORD_1 src1_sel:WORD_1
	v_cndmask_b32_e64 v41, v138, v162, s[64:65]
	s_mov_b64 vcc, s[66:67]
	v_cndmask_b32_sdwa v41, v138, v162, vcc dst_sel:WORD_1 dst_unused:UNUSED_PRESERVE src0_sel:WORD_1 src1_sel:WORD_1
	v_mfma_f32_32x32x16_f16 a[160:175], v[110:113], v[70:73], a[160:175]
	v_pk_add_f16 v148, v19, v18
	v_pk_add_f16 v149, v20, v21
	v_mfma_f32_32x32x16_f16 a[128:143], v[114:117], v[78:81], a[128:143]
	v_pk_add_f16 v150, v39, v38
	v_pk_add_f16 v151, v40, v41
	v_mfma_f32_32x32x16_f16 a[144:159], v[110:113], v[78:81], a[144:159]
	v_pk_add_f16 v148, v148, v149
	v_pk_add_f16 v150, v150, v151
	v_mfma_f32_32x32x16_f16 a[80:95], v[114:117], v[102:105], a[80:95]
	v_fma_mix_f32 v134, v148, 1.0, v134 op_sel_hi:[1,0,0]
	v_fma_mix_f32 v135, v150, 1.0, v135 op_sel_hi:[1,0,0]
	v_mfma_f32_32x32x16_f16 a[96:111], v[110:113], v[102:105], a[96:111]
	v_fma_mix_f32 v134, v148, 1.0, v134 op_sel:[1,0,0] op_sel_hi:[1,0,0]
	v_fma_mix_f32 v135, v150, 1.0, v135 op_sel:[1,0,0] op_sel_hi:[1,0,0]
	s_waitcnt lgkmcnt(0)
	v_mfma_f32_32x32x16_f16 a[0:15], v[18:21], v[74:77], a[0:15]
	v_mfma_f32_32x32x16_f16 a[240:255], v[38:41], v[74:77], a[240:255]
	ds_read_b128 v[50:53], v210
	v_pk_mul_f16 v148, v46, v136
	v_pk_mul_f16 v149, v42, v137
	v_pk_mul_f16 v150, v47, v136
	v_pk_mul_f16 v151, v43, v137
	v_mfma_f32_32x32x16_f16 a[16:31], v[18:21], v[126:129], a[16:31]
	ds_read_b128 v[54:57], v210 offset:4096
	v_pk_mul_f16 v152, v48, v136
	v_pk_mul_f16 v153, v44, v137
	v_pk_mul_f16 v154, v49, v136
	v_pk_mul_f16 v155, v45, v137
	v_mfma_f32_32x32x16_f16 a[224:239], v[38:41], v[126:129], a[224:239]
	ds_read_b128 v[58:61], v210 offset:8192
	v_pk_mul_f16 v156, v46, v140
	v_pk_mul_f16 v157, v42, v139
	v_pk_mul_f16 v158, v47, v140
	v_pk_mul_f16 v159, v43, v139
	v_mfma_f32_32x32x16_f16 a[32:47], v[18:21], v[122:125], a[32:47]
	ds_read_b128 v[62:65], v210 offset:12288
	v_pk_mul_f16 v160, v48, v140
	v_pk_mul_f16 v161, v44, v139
	v_pk_mul_f16 v162, v49, v140
	v_pk_mul_f16 v163, v45, v139
	v_mfma_f32_32x32x16_f16 a[208:223], v[38:41], v[122:125], a[208:223]
	ds_read_b128 v[66:69], v210 offset:16384
	v_pk_max_f16 v148, v148, v149
	v_pk_max_f16 v150, v150, v151
	v_pk_max_f16 v152, v152, v153
	v_pk_max_f16 v154, v154, v155
	v_mfma_f32_32x32x16_f16 a[48:63], v[18:21], v[118:121], a[48:63]
	ds_read_b128 v[70:73], v210 offset:20480
	v_pk_max_f16 v156, v156, v157
	v_pk_max_f16 v158, v158, v159
	v_pk_max_f16 v160, v160, v161
	v_pk_max_f16 v162, v162, v163
	v_mfma_f32_32x32x16_f16 a[192:207], v[38:41], v[118:121], a[192:207]
	ds_read_b128 v[78:81], v210 offset:24576
	v_cndmask_b32_e64 v114, v1, v148, s[36:37]
	s_mov_b64 vcc, s[38:39]
	v_cndmask_b32_sdwa v114, v1, v148, vcc dst_sel:WORD_1 dst_unused:UNUSED_PRESERVE src0_sel:WORD_1 src1_sel:WORD_1
	v_cndmask_b32_e64 v115, v1, v150, s[40:41]
	s_mov_b64 vcc, s[42:43]
	v_cndmask_b32_sdwa v115, v1, v150, vcc dst_sel:WORD_1 dst_unused:UNUSED_PRESERVE src0_sel:WORD_1 src1_sel:WORD_1
	v_mfma_f32_32x32x16_f16 a[64:79], v[18:21], v[106:109], a[64:79]
	ds_read_b128 v[102:105], v210 offset:28672
	v_cndmask_b32_e64 v116, v1, v152, s[44:45]
	s_mov_b64 vcc, s[46:47]
	v_cndmask_b32_sdwa v116, v1, v152, vcc dst_sel:WORD_1 dst_unused:UNUSED_PRESERVE src0_sel:WORD_1 src1_sel:WORD_1
	v_cndmask_b32_e64 v117, v1, v154, s[48:49]
	s_mov_b64 vcc, s[50:51]
	v_cndmask_b32_sdwa v117, v1, v154, vcc dst_sel:WORD_1 dst_unused:UNUSED_PRESERVE src0_sel:WORD_1 src1_sel:WORD_1
	v_mfma_f32_32x32x16_f16 a[176:191], v[38:41], v[106:109], a[176:191]
	v_cndmask_b32_e64 v110, v138, v156, s[4:5]
	s_mov_b64 vcc, s[6:7]
	v_cndmask_b32_sdwa v110, v138, v156, vcc dst_sel:WORD_1 dst_unused:UNUSED_PRESERVE src0_sel:WORD_1 src1_sel:WORD_1
	v_cndmask_b32_e64 v111, v138, v158, s[8:9]
	s_mov_b64 vcc, s[10:11]
	v_cndmask_b32_sdwa v111, v138, v158, vcc dst_sel:WORD_1 dst_unused:UNUSED_PRESERVE src0_sel:WORD_1 src1_sel:WORD_1
	v_mfma_f32_32x32x16_f16 a[112:127], v[18:21], v[98:101], a[112:127]
	v_cndmask_b32_e64 v112, v138, v160, s[12:13]
	s_mov_b64 vcc, s[14:15]
	v_cndmask_b32_sdwa v112, v138, v160, vcc dst_sel:WORD_1 dst_unused:UNUSED_PRESERVE src0_sel:WORD_1 src1_sel:WORD_1
	v_cndmask_b32_e64 v113, v138, v162, s[16:17]
	s_mov_b64 vcc, s[18:19]
	v_cndmask_b32_sdwa v113, v138, v162, vcc dst_sel:WORD_1 dst_unused:UNUSED_PRESERVE src0_sel:WORD_1 src1_sel:WORD_1
	v_mfma_f32_32x32x16_f16 a[160:175], v[38:41], v[98:101], a[160:175]
	v_pk_add_f16 v148, v115, v114
	v_pk_add_f16 v149, v116, v117
	v_mfma_f32_32x32x16_f16 a[128:143], v[18:21], v[94:97], a[128:143]
	v_pk_add_f16 v150, v111, v110
	v_pk_add_f16 v151, v112, v113
	v_mfma_f32_32x32x16_f16 a[144:159], v[38:41], v[94:97], a[144:159]
	v_pk_add_f16 v148, v148, v149
	v_pk_add_f16 v150, v150, v151
	v_mfma_f32_32x32x16_f16 a[80:95], v[18:21], v[86:89], a[80:95]
	v_fma_mix_f32 v134, v148, 1.0, v134 op_sel_hi:[1,0,0]
	v_fma_mix_f32 v135, v150, 1.0, v135 op_sel_hi:[1,0,0]
	v_mfma_f32_32x32x16_f16 a[96:111], v[38:41], v[86:89], a[96:111]
	v_fma_mix_f32 v134, v148, 1.0, v134 op_sel:[1,0,0] op_sel_hi:[1,0,0]
	v_fma_mix_f32 v135, v150, 1.0, v135 op_sel:[1,0,0] op_sel_hi:[1,0,0]
	s_waitcnt lgkmcnt(0)
	v_mfma_f32_32x32x16_f16 a[0:15], v[114:117], v[50:53], a[0:15]
	v_mfma_f32_32x32x16_f16 a[240:255], v[110:113], v[50:53], a[240:255]
	v_mfma_f32_32x32x16_f16 a[16:31], v[114:117], v[54:57], a[16:31]
	v_mfma_f32_32x32x16_f16 a[224:239], v[110:113], v[54:57], a[224:239]
	v_mfma_f32_32x32x16_f16 a[32:47], v[114:117], v[58:61], a[32:47]
	v_mfma_f32_32x32x16_f16 a[208:223], v[110:113], v[58:61], a[208:223]
	v_mfma_f32_32x32x16_f16 a[48:63], v[114:117], v[62:65], a[48:63]
	v_mfma_f32_32x32x16_f16 a[192:207], v[110:113], v[62:65], a[192:207]
	v_mfma_f32_32x32x16_f16 a[64:79], v[114:117], v[66:69], a[64:79]
	v_mfma_f32_32x32x16_f16 a[176:191], v[110:113], v[66:69], a[176:191]
	v_mfma_f32_32x32x16_f16 a[112:127], v[114:117], v[70:73], a[112:127]
	v_mfma_f32_32x32x16_f16 a[160:175], v[110:113], v[70:73], a[160:175]
	v_mfma_f32_32x32x16_f16 a[128:143], v[114:117], v[78:81], a[128:143]
	v_mfma_f32_32x32x16_f16 a[144:159], v[110:113], v[78:81], a[144:159]
	v_mfma_f32_32x32x16_f16 a[80:95], v[114:117], v[102:105], a[80:95]
	v_mfma_f32_32x32x16_f16 a[96:111], v[110:113], v[102:105], a[96:111]
	v_readfirstlane_b32 s1, v0
	s_and_b32 s0, s3, 0xffffff00
	s_andn2_b32 s1, s1, 63
	s_add_i32 s4, s1, s0
	s_lshl_b32 s0, s2, 13
	s_and_b32 s6, s0, 0xe000
	s_ashr_i32 s5, s4, 31
	s_add_u32 s0, s4, s6
	s_addc_u32 s1, s5, 0
	s_lshl_b64 s[2:3], s[0:1], 9
	v_lshrrev_b32_e32 v0, 3, v132
	s_add_u32 s2, s22, s2
	v_and_b32_e32 v3, 12, v0
	s_addc_u32 s3, s23, s3
	v_lshlrev_b32_e32 v0, 9, v3
	v_mov_b32_e32 v1, 0
	v_lshl_add_u64 v[4:5], s[2:3], 0, v[0:1]
	v_lshlrev_b32_e32 v0, 4, v132
	v_and_b32_e32 v0, 0x1f0, v0
	v_lshl_add_u64 v[4:5], v[4:5], 0, v[0:1]
	v_accvgpr_read_b32 v6, a0
	v_accvgpr_read_b32 v7, a16
	v_accvgpr_read_b32 v8, a32
	v_max3_f32 v0, |v6|, |v7|, |v8|
	v_accvgpr_read_b32 v9, a48
	v_accvgpr_read_b32 v14, a64
	v_max3_f32 v0, |v0|, |v9|, |v14|
	v_accvgpr_read_b32 v15, a112
	v_accvgpr_read_b32 v16, a128
	v_max3_f32 v0, |v0|, |v15|, |v16|
	v_accvgpr_read_b32 v17, a80
	v_max3_f32 v10, |v0|, |v17|, |v17|
	v_accvgpr_read_b32 v18, a1
	v_accvgpr_read_b32 v19, a17
	v_accvgpr_read_b32 v20, a33
	v_max3_f32 v0, |v18|, |v19|, |v20|
	v_accvgpr_read_b32 v21, a49
	v_accvgpr_read_b32 v22, a65
	v_max3_f32 v0, |v0|, |v21|, |v22|
	v_accvgpr_read_b32 v23, a113
	v_accvgpr_read_b32 v24, a129
	v_max3_f32 v0, |v0|, |v23|, |v24|
	v_accvgpr_read_b32 v25, a81
	v_max3_f32 v11, |v0|, |v25|, |v25|
	v_accvgpr_read_b32 v26, a2
	v_accvgpr_read_b32 v27, a18
	v_accvgpr_read_b32 v28, a34
	v_max3_f32 v0, |v26|, |v27|, |v28|
	v_accvgpr_read_b32 v29, a50
	v_accvgpr_read_b32 v30, a66
	v_max3_f32 v0, |v0|, |v29|, |v30|
	v_accvgpr_read_b32 v31, a114
	v_accvgpr_read_b32 v32, a130
	v_max3_f32 v0, |v0|, |v31|, |v32|
	v_accvgpr_read_b32 v33, a82
	v_max3_f32 v12, |v0|, |v33|, |v33|
	v_accvgpr_read_b32 v34, a3
	v_accvgpr_read_b32 v35, a19
	v_accvgpr_read_b32 v36, a35
	v_max3_f32 v0, |v34|, |v35|, |v36|
	v_accvgpr_read_b32 v37, a51
	v_accvgpr_read_b32 v38, a67
	v_max3_f32 v0, |v0|, |v37|, |v38|
	v_accvgpr_read_b32 v39, a115
	v_accvgpr_read_b32 v40, a131
	v_max3_f32 v0, |v0|, |v39|, |v40|
	v_accvgpr_read_b32 v41, a83
	v_max3_f32 v13, |v0|, |v41|, |v41|
	v_lshlrev_b32_e32 v0, 2, v3
	s_nop 1
	v_max_f32_dpp v10, v10, v10 quad_perm:[1,0,3,2] row_mask:0xf bank_mask:0xf
	v_max_f32_dpp v11, v11, v11 quad_perm:[1,0,3,2] row_mask:0xf bank_mask:0xf
	v_max_f32_dpp v12, v12, v12 quad_perm:[1,0,3,2] row_mask:0xf bank_mask:0xf
	v_max_f32_dpp v13, v13, v13 quad_perm:[1,0,3,2] row_mask:0xf bank_mask:0xf
	v_max_f32_dpp v10, v10, v10 quad_perm:[2,3,0,1] row_mask:0xf bank_mask:0xf
	v_max_f32_dpp v11, v11, v11 quad_perm:[2,3,0,1] row_mask:0xf bank_mask:0xf
	v_max_f32_dpp v12, v12, v12 quad_perm:[2,3,0,1] row_mask:0xf bank_mask:0xf
	v_max_f32_dpp v13, v13, v13 quad_perm:[2,3,0,1] row_mask:0xf bank_mask:0xf
	v_max_f32_dpp v10, v10, v10 row_half_mirror row_mask:0xf bank_mask:0xf
	v_max_f32_dpp v11, v11, v11 row_half_mirror row_mask:0xf bank_mask:0xf
	v_max_f32_dpp v12, v12, v12 row_half_mirror row_mask:0xf bank_mask:0xf
	v_max_f32_dpp v13, v13, v13 row_half_mirror row_mask:0xf bank_mask:0xf
	v_max_f32_dpp v10, v10, v10 row_mirror row_mask:0xf bank_mask:0xf
	v_max_f32_dpp v11, v11, v11 row_mirror row_mask:0xf bank_mask:0xf
	v_max_f32_dpp v12, v12, v12 row_mirror row_mask:0xf bank_mask:0xf
	v_max_f32_dpp v13, v13, v13 row_mirror row_mask:0xf bank_mask:0xf
	s_nop 0
	ds_swizzle_b32 v232, v10 offset:swizzle(SWAP,16)
	ds_swizzle_b32 v233, v12 offset:swizzle(SWAP,16)
	ds_swizzle_b32 v234, v11 offset:swizzle(SWAP,16)
	ds_swizzle_b32 v235, v13 offset:swizzle(SWAP,16)
	s_waitcnt lgkmcnt(0)
	v_max_f32_e32 v10, v10, v232
	v_rcp_f32_e32 v42, v10
	v_cmp_lt_f32_e32 vcc, 0, v10
	s_waitcnt lgkmcnt(0)
	v_max_f32_e32 v12, v12, v233
	s_waitcnt lgkmcnt(0)
	v_max_f32_e32 v11, v11, v234
	s_lshl_b32 s2, s6, 2
	v_cndmask_b32_e32 v3, 0, v42, vcc
	v_pk_mul_f32 v[224:225], v[6:7], v[2:3] op_sel:[0,1] op_sel_hi:[1,1]
	v_pk_mul_f32 v[226:227], v[8:9], v[2:3] op_sel:[0,1] op_sel_hi:[1,1]
	v_cvt_pknorm_i16_f32 v6, v224, v225
	v_cvt_pknorm_i16_f32 v7, v226, v227
	v_pk_mul_f32 v[228:229], v[14:15], v[2:3] op_sel:[0,1] op_sel_hi:[1,1]
	v_rcp_f32_e32 v14, v11
	v_cvt_pknorm_i16_f32 v8, v228, v229
	v_pk_mul_f32 v[230:231], v[16:17], v[2:3] op_sel:[0,1] op_sel_hi:[1,1]
	v_cmp_lt_f32_e32 vcc, 0, v11
	v_cvt_pknorm_i16_f32 v9, v230, v231
	global_store_dwordx4 v[4:5], v[6:9], off sc0 sc1
	s_add_u32 s6, s24, s2
	v_cndmask_b32_e32 v3, 0, v14, vcc
	v_pk_mul_f32 v[224:225], v[18:19], v[2:3] op_sel:[0,1] op_sel_hi:[1,1]
	v_pk_mul_f32 v[226:227], v[20:21], v[2:3] op_sel:[0,1] op_sel_hi:[1,1]
	v_cvt_pknorm_i16_f32 v6, v224, v225
	v_cvt_pknorm_i16_f32 v7, v226, v227
	v_pk_mul_f32 v[228:229], v[22:23], v[2:3] op_sel:[0,1] op_sel_hi:[1,1]
	v_pk_mul_f32 v[230:231], v[24:25], v[2:3] op_sel:[0,1] op_sel_hi:[1,1]
	v_cvt_pknorm_i16_f32 v8, v228, v229
	v_cvt_pknorm_i16_f32 v9, v230, v231
	v_rcp_f32_e32 v3, v12
	s_addc_u32 s7, s25, 0
	s_lshl_b64 s[2:3], s[4:5], 2
	s_mov_b64 s[4:5], 0x200
	s_add_u32 s2, s6, s2
	v_lshl_add_u64 v[14:15], v[4:5], 0, s[4:5]
	s_mov_b32 s4, 0x38000100
	v_cmp_lt_f32_e32 vcc, 0, v12
	s_addc_u32 s3, s7, s3
	global_store_dwordx4 v[14:15], v[6:9], off sc0 sc1
	s_nop 1
	v_pk_mul_f32 v[6:7], v[10:11], s[4:5] op_sel_hi:[1,0]
	v_cndmask_b32_e32 v3, 0, v3, vcc
	global_store_dwordx2 v0, v[6:7], s[2:3]
	v_pk_mul_f32 v[224:225], v[26:27], v[2:3] op_sel:[0,1] op_sel_hi:[1,1]
	v_pk_mul_f32 v[226:227], v[28:29], v[2:3] op_sel:[0,1] op_sel_hi:[1,1]
	v_cvt_pknorm_i16_f32 v6, v224, v225
	v_cvt_pknorm_i16_f32 v7, v226, v227
	v_pk_mul_f32 v[228:229], v[30:31], v[2:3] op_sel:[0,1] op_sel_hi:[1,1]
	v_pk_mul_f32 v[230:231], v[32:33], v[2:3] op_sel:[0,1] op_sel_hi:[1,1]
	v_cvt_pknorm_i16_f32 v8, v228, v229
	s_waitcnt lgkmcnt(0)
	v_max_f32_e32 v13, v13, v235
	v_cvt_pknorm_i16_f32 v9, v230, v231
	v_rcp_f32_e32 v3, v13
	v_cmp_lt_f32_e32 vcc, 0, v13
	s_mov_b64 s[6:7], 0x400
	v_lshl_add_u64 v[10:11], v[4:5], 0, s[6:7]
	v_cndmask_b32_e32 v3, 0, v3, vcc
	global_store_dwordx4 v[10:11], v[6:9], off sc0 sc1
	v_pk_mul_f32 v[224:225], v[34:35], v[2:3] op_sel:[0,1] op_sel_hi:[1,1]
	v_pk_mul_f32 v[226:227], v[36:37], v[2:3] op_sel:[0,1] op_sel_hi:[1,1]
	v_cvt_pknorm_i16_f32 v6, v224, v225
	v_cvt_pknorm_i16_f32 v7, v226, v227
	v_pk_mul_f32 v[228:229], v[38:39], v[2:3] op_sel:[0,1] op_sel_hi:[1,1]
	v_pk_mul_f32 v[230:231], v[40:41], v[2:3] op_sel:[0,1] op_sel_hi:[1,1]
	v_cvt_pknorm_i16_f32 v8, v228, v229
	s_mov_b64 s[6:7], 0x600
	v_cvt_pknorm_i16_f32 v9, v230, v231
	v_lshl_add_u64 v[10:11], v[4:5], 0, s[6:7]
	global_store_dwordx4 v[10:11], v[6:9], off sc0 sc1
	s_nop 1
	v_pk_mul_f32 v[6:7], v[12:13], s[4:5] op_sel_hi:[1,0]
	v_lshlrev_b32_e32 v2, 2, v132
	global_store_dwordx2 v0, v[6:7], s[2:3] offset:8
	v_accvgpr_read_b32 v42, a4
	v_accvgpr_read_b32 v6, a20
	v_accvgpr_read_b32 v7, a36
	v_max3_f32 v8, |v42|, |v6|, |v7|
	v_accvgpr_read_b32 v9, a52
	v_accvgpr_read_b32 v14, a68
	v_max3_f32 v8, |v8|, |v9|, |v14|
	v_accvgpr_read_b32 v15, a116
	v_accvgpr_read_b32 v16, a132
	v_max3_f32 v8, |v8|, |v15|, |v16|
	v_accvgpr_read_b32 v10, a84
	v_accvgpr_read_b32 v43, a5
	v_accvgpr_read_b32 v17, a84
	v_max3_f32 v8, |v8|, |v17|, |v10|
	v_accvgpr_read_b32 v19, a21
	v_accvgpr_read_b32 v20, a37
	v_max3_f32 v10, |v43|, |v19|, |v20|
	v_accvgpr_read_b32 v21, a53
	v_accvgpr_read_b32 v22, a69
	v_max3_f32 v10, |v10|, |v21|, |v22|
	v_accvgpr_read_b32 v23, a117
	v_accvgpr_read_b32 v24, a133
	v_max3_f32 v10, |v10|, |v23|, |v24|
	v_accvgpr_read_b32 v44, a6
	v_accvgpr_read_b32 v25, a85
	v_max3_f32 v11, |v10|, |v25|, |v25|
	v_accvgpr_read_b32 v27, a22
	v_accvgpr_read_b32 v28, a38
	v_max3_f32 v10, |v44|, |v27|, |v28|
	v_accvgpr_read_b32 v29, a54
	v_accvgpr_read_b32 v30, a70
	v_max3_f32 v10, |v10|, |v29|, |v30|
	v_accvgpr_read_b32 v31, a118
	v_accvgpr_read_b32 v32, a134
	v_max3_f32 v10, |v10|, |v31|, |v32|
	v_accvgpr_read_b32 v45, a7
	v_accvgpr_read_b32 v33, a86
	v_max3_f32 v12, |v10|, |v33|, |v33|
	v_accvgpr_read_b32 v35, a23
	v_accvgpr_read_b32 v36, a39
	v_max3_f32 v10, |v45|, |v35|, |v36|
	v_accvgpr_read_b32 v37, a55
	v_accvgpr_read_b32 v38, a71
	v_max3_f32 v10, |v10|, |v37|, |v38|
	v_accvgpr_read_b32 v39, a119
	v_accvgpr_read_b32 v40, a135
	v_max3_f32 v10, |v10|, |v39|, |v40|
	v_accvgpr_read_b32 v41, a87
	v_max3_f32 v13, |v10|, |v41|, |v41|
	v_mov_b32_e32 v3, v42
	s_nop 1
	v_max_f32_dpp v8, v8, v8 quad_perm:[1,0,3,2] row_mask:0xf bank_mask:0xf
	v_max_f32_dpp v11, v11, v11 quad_perm:[1,0,3,2] row_mask:0xf bank_mask:0xf
	v_max_f32_dpp v12, v12, v12 quad_perm:[1,0,3,2] row_mask:0xf bank_mask:0xf
	v_max_f32_dpp v13, v13, v13 quad_perm:[1,0,3,2] row_mask:0xf bank_mask:0xf
	v_max_f32_dpp v8, v8, v8 quad_perm:[2,3,0,1] row_mask:0xf bank_mask:0xf
	v_max_f32_dpp v11, v11, v11 quad_perm:[2,3,0,1] row_mask:0xf bank_mask:0xf
	v_max_f32_dpp v12, v12, v12 quad_perm:[2,3,0,1] row_mask:0xf bank_mask:0xf
	v_max_f32_dpp v13, v13, v13 quad_perm:[2,3,0,1] row_mask:0xf bank_mask:0xf
	v_max_f32_dpp v8, v8, v8 row_half_mirror row_mask:0xf bank_mask:0xf
	v_max_f32_dpp v11, v11, v11 row_half_mirror row_mask:0xf bank_mask:0xf
	v_max_f32_dpp v12, v12, v12 row_half_mirror row_mask:0xf bank_mask:0xf
	v_max_f32_dpp v13, v13, v13 row_half_mirror row_mask:0xf bank_mask:0xf
	v_max_f32_dpp v8, v8, v8 row_mirror row_mask:0xf bank_mask:0xf
	v_max_f32_dpp v11, v11, v11 row_mirror row_mask:0xf bank_mask:0xf
	v_max_f32_dpp v12, v12, v12 row_mirror row_mask:0xf bank_mask:0xf
	v_max_f32_dpp v13, v13, v13 row_mirror row_mask:0xf bank_mask:0xf
	s_nop 0
	ds_swizzle_b32 v232, v8 offset:swizzle(SWAP,16)
	ds_swizzle_b32 v233, v11 offset:swizzle(SWAP,16)
	ds_swizzle_b32 v234, v12 offset:swizzle(SWAP,16)
	ds_swizzle_b32 v235, v13 offset:swizzle(SWAP,16)
	s_waitcnt lgkmcnt(0)
	v_max_f32_e32 v10, v8, v232
	v_rcp_f32_e32 v8, v10
	v_cmp_lt_f32_e32 vcc, 0, v10
	s_waitcnt lgkmcnt(0)
	v_max_f32_e32 v11, v11, v233
	v_mov_b32_e32 v18, v43
	s_mov_b64 s[6:7], 0x1000
	v_cndmask_b32_e32 v42, 0, v8, vcc
	v_mul_f32_e32 v3, v42, v3
	v_mul_f32_e32 v6, v42, v6
	v_cvt_pknorm_i16_f32 v6, v3, v6
	v_mul_f32_e32 v3, v42, v7
	v_mul_f32_e32 v7, v42, v9
	v_cvt_pknorm_i16_f32 v7, v3, v7
	v_pk_mul_f32 v[224:225], v[14:15], v[42:43] op_sel_hi:[1,0]
	v_pk_mul_f32 v[226:227], v[16:17], v[42:43] op_sel_hi:[1,0]
	v_cvt_pknorm_i16_f32 v8, v224, v225
	v_cvt_pknorm_i16_f32 v9, v226, v227
	v_rcp_f32_e32 v3, v11
	v_cmp_lt_f32_e32 vcc, 0, v11
	v_lshl_add_u64 v[14:15], v[4:5], 0, s[6:7]
	global_store_dwordx4 v[14:15], v[6:9], off sc0 sc1
	v_cndmask_b32_e32 v3, 0, v3, vcc
	v_pk_mul_f32 v[228:229], v[18:19], v[2:3] op_sel:[0,1] op_sel_hi:[1,1]
	v_pk_mul_f32 v[230:231], v[20:21], v[2:3] op_sel:[0,1] op_sel_hi:[1,1]
	v_cvt_pknorm_i16_f32 v6, v228, v229
	v_cvt_pknorm_i16_f32 v7, v230, v231
	v_pk_mul_f32 v[224:225], v[22:23], v[2:3] op_sel:[0,1] op_sel_hi:[1,1]
	v_pk_mul_f32 v[226:227], v[24:25], v[2:3] op_sel:[0,1] op_sel_hi:[1,1]
	v_cvt_pknorm_i16_f32 v8, v224, v225
	s_waitcnt lgkmcnt(0)
	v_max_f32_e32 v12, v12, v234
	v_cvt_pknorm_i16_f32 v9, v226, v227
	v_rcp_f32_e32 v3, v12
	s_mov_b64 s[6:7], 0x1200
	v_cmp_lt_f32_e32 vcc, 0, v12
	v_mov_b32_e32 v26, v44
	v_lshl_add_u64 v[14:15], v[4:5], 0, s[6:7]
	global_store_dwordx4 v[14:15], v[6:9], off sc0 sc1
	s_nop 1
	v_pk_mul_f32 v[6:7], v[10:11], s[4:5] op_sel_hi:[1,0]
	v_cndmask_b32_e32 v3, 0, v3, vcc
	global_store_dwordx2 v0, v[6:7], s[2:3] offset:32
	v_pk_mul_f32 v[228:229], v[26:27], v[2:3] op_sel:[0,1] op_sel_hi:[1,1]
	v_pk_mul_f32 v[230:231], v[28:29], v[2:3] op_sel:[0,1] op_sel_hi:[1,1]
	v_cvt_pknorm_i16_f32 v6, v228, v229
	v_cvt_pknorm_i16_f32 v7, v230, v231
	v_pk_mul_f32 v[224:225], v[30:31], v[2:3] op_sel:[0,1] op_sel_hi:[1,1]
	v_pk_mul_f32 v[226:227], v[32:33], v[2:3] op_sel:[0,1] op_sel_hi:[1,1]
	v_cvt_pknorm_i16_f32 v8, v224, v225
	s_waitcnt lgkmcnt(0)
	v_max_f32_e32 v13, v13, v235
	v_cvt_pknorm_i16_f32 v9, v226, v227
	v_rcp_f32_e32 v3, v13
	v_cmp_lt_f32_e32 vcc, 0, v13
	v_mov_b32_e32 v34, v45
	s_mov_b64 s[6:7], 0x1400
	v_cndmask_b32_e32 v3, 0, v3, vcc
	v_lshl_add_u64 v[10:11], v[4:5], 0, s[6:7]
	global_store_dwordx4 v[10:11], v[6:9], off sc0 sc1
	v_pk_mul_f32 v[228:229], v[34:35], v[2:3] op_sel:[0,1] op_sel_hi:[1,1]
	v_pk_mul_f32 v[230:231], v[36:37], v[2:3] op_sel:[0,1] op_sel_hi:[1,1]
	v_cvt_pknorm_i16_f32 v6, v228, v229
	v_cvt_pknorm_i16_f32 v7, v230, v231
	v_pk_mul_f32 v[224:225], v[38:39], v[2:3] op_sel:[0,1] op_sel_hi:[1,1]
	v_pk_mul_f32 v[226:227], v[40:41], v[2:3] op_sel:[0,1] op_sel_hi:[1,1]
	v_cvt_pknorm_i16_f32 v8, v224, v225
	s_mov_b64 s[6:7], 0x1600
	v_cvt_pknorm_i16_f32 v9, v226, v227
	v_lshl_add_u64 v[10:11], v[4:5], 0, s[6:7]
	global_store_dwordx4 v[10:11], v[6:9], off sc0 sc1
	s_nop 1
	v_pk_mul_f32 v[6:7], v[12:13], s[4:5] op_sel_hi:[1,0]
	v_accvgpr_read_b32 v46, a8
	v_accvgpr_read_b32 v47, a9
	v_accvgpr_read_b32 v48, a10
	v_accvgpr_read_b32 v49, a11
	v_accvgpr_read_b32 v50, a12
	v_accvgpr_read_b32 v51, a13
	v_accvgpr_read_b32 v52, a14
	v_accvgpr_read_b32 v53, a15
	global_store_dwordx2 v0, v[6:7], s[2:3] offset:40
	v_mov_b64_e32 v[42:43], v[46:47]
	v_accvgpr_read_b32 v6, a24
	v_accvgpr_read_b32 v7, a40
	v_max3_f32 v8, |v42|, |v6|, |v7|
	v_accvgpr_read_b32 v9, a56
	v_accvgpr_read_b32 v14, a72
	v_max3_f32 v8, |v8|, |v9|, |v14|
	v_accvgpr_read_b32 v15, a120
	v_accvgpr_read_b32 v16, a136
	v_max3_f32 v8, |v8|, |v15|, |v16|
	v_accvgpr_read_b32 v10, a88
	v_accvgpr_read_b32 v17, a88
	v_max3_f32 v8, |v8|, |v17|, |v10|
	v_accvgpr_read_b32 v19, a25
	v_accvgpr_read_b32 v20, a41
	v_max3_f32 v10, |v43|, |v19|, |v20|
	v_accvgpr_read_b32 v21, a57
	v_accvgpr_read_b32 v22, a73
	v_max3_f32 v10, |v10|, |v21|, |v22|
	v_accvgpr_read_b32 v23, a121
	v_accvgpr_read_b32 v24, a137
	v_max3_f32 v10, |v10|, |v23|, |v24|
	v_mov_b64_e32 v[44:45], v[48:49]
	v_accvgpr_read_b32 v25, a89
	v_max3_f32 v11, |v10|, |v25|, |v25|
	v_accvgpr_read_b32 v27, a26
	v_accvgpr_read_b32 v28, a42
	v_max3_f32 v10, |v44|, |v27|, |v28|
	v_accvgpr_read_b32 v29, a58
	v_accvgpr_read_b32 v30, a74
	v_max3_f32 v10, |v10|, |v29|, |v30|
	v_accvgpr_read_b32 v31, a122
	v_accvgpr_read_b32 v32, a138
	v_max3_f32 v10, |v10|, |v31|, |v32|
	v_accvgpr_read_b32 v33, a90
	v_max3_f32 v12, |v10|, |v33|, |v33|
	v_accvgpr_read_b32 v35, a27
	v_accvgpr_read_b32 v36, a43
	v_max3_f32 v10, |v45|, |v35|, |v36|
	v_accvgpr_read_b32 v37, a59
	v_accvgpr_read_b32 v38, a75
	v_max3_f32 v10, |v10|, |v37|, |v38|
	v_accvgpr_read_b32 v39, a123
	v_accvgpr_read_b32 v40, a139
	v_max3_f32 v10, |v10|, |v39|, |v40|
	v_accvgpr_read_b32 v41, a91
	v_max3_f32 v13, |v10|, |v41|, |v41|
	v_mov_b32_e32 v3, v42
	s_nop 1
	v_max_f32_dpp v8, v8, v8 quad_perm:[1,0,3,2] row_mask:0xf bank_mask:0xf
	v_max_f32_dpp v11, v11, v11 quad_perm:[1,0,3,2] row_mask:0xf bank_mask:0xf
	v_max_f32_dpp v12, v12, v12 quad_perm:[1,0,3,2] row_mask:0xf bank_mask:0xf
	v_max_f32_dpp v13, v13, v13 quad_perm:[1,0,3,2] row_mask:0xf bank_mask:0xf
	v_max_f32_dpp v8, v8, v8 quad_perm:[2,3,0,1] row_mask:0xf bank_mask:0xf
	v_max_f32_dpp v11, v11, v11 quad_perm:[2,3,0,1] row_mask:0xf bank_mask:0xf
	v_max_f32_dpp v12, v12, v12 quad_perm:[2,3,0,1] row_mask:0xf bank_mask:0xf
	v_max_f32_dpp v13, v13, v13 quad_perm:[2,3,0,1] row_mask:0xf bank_mask:0xf
	v_max_f32_dpp v8, v8, v8 row_half_mirror row_mask:0xf bank_mask:0xf
	v_max_f32_dpp v11, v11, v11 row_half_mirror row_mask:0xf bank_mask:0xf
	v_max_f32_dpp v12, v12, v12 row_half_mirror row_mask:0xf bank_mask:0xf
	v_max_f32_dpp v13, v13, v13 row_half_mirror row_mask:0xf bank_mask:0xf
	v_max_f32_dpp v8, v8, v8 row_mirror row_mask:0xf bank_mask:0xf
	v_max_f32_dpp v11, v11, v11 row_mirror row_mask:0xf bank_mask:0xf
	v_max_f32_dpp v12, v12, v12 row_mirror row_mask:0xf bank_mask:0xf
	v_max_f32_dpp v13, v13, v13 row_mirror row_mask:0xf bank_mask:0xf
	s_nop 0
	ds_swizzle_b32 v232, v8 offset:swizzle(SWAP,16)
	ds_swizzle_b32 v233, v11 offset:swizzle(SWAP,16)
	ds_swizzle_b32 v234, v12 offset:swizzle(SWAP,16)
	ds_swizzle_b32 v235, v13 offset:swizzle(SWAP,16)
	s_waitcnt lgkmcnt(0)
	v_max_f32_e32 v10, v8, v232
	v_rcp_f32_e32 v8, v10
	v_cmp_lt_f32_e32 vcc, 0, v10
	s_waitcnt lgkmcnt(0)
	v_max_f32_e32 v11, v11, v233
	v_mov_b32_e32 v18, v43
	s_mov_b64 s[6:7], 0x2000
	v_cndmask_b32_e32 v42, 0, v8, vcc
	v_mul_f32_e32 v3, v42, v3
	v_mul_f32_e32 v6, v42, v6
	v_cvt_pknorm_i16_f32 v6, v3, v6
	v_mul_f32_e32 v3, v42, v7
	v_mul_f32_e32 v7, v42, v9
	v_cvt_pknorm_i16_f32 v7, v3, v7
	v_pk_mul_f32 v[228:229], v[14:15], v[42:43] op_sel_hi:[1,0]
	v_pk_mul_f32 v[230:231], v[16:17], v[42:43] op_sel_hi:[1,0]
	v_cvt_pknorm_i16_f32 v8, v228, v229
	v_cvt_pknorm_i16_f32 v9, v230, v231
	v_rcp_f32_e32 v3, v11
	v_cmp_lt_f32_e32 vcc, 0, v11
	v_lshl_add_u64 v[14:15], v[4:5], 0, s[6:7]
	global_store_dwordx4 v[14:15], v[6:9], off sc0 sc1
	v_cndmask_b32_e32 v3, 0, v3, vcc
	v_pk_mul_f32 v[224:225], v[18:19], v[2:3] op_sel:[0,1] op_sel_hi:[1,1]
	v_pk_mul_f32 v[226:227], v[20:21], v[2:3] op_sel:[0,1] op_sel_hi:[1,1]
	v_cvt_pknorm_i16_f32 v6, v224, v225
	v_cvt_pknorm_i16_f32 v7, v226, v227
	v_pk_mul_f32 v[228:229], v[22:23], v[2:3] op_sel:[0,1] op_sel_hi:[1,1]
	v_pk_mul_f32 v[230:231], v[24:25], v[2:3] op_sel:[0,1] op_sel_hi:[1,1]
	v_cvt_pknorm_i16_f32 v8, v228, v229
	s_waitcnt lgkmcnt(0)
	v_max_f32_e32 v12, v12, v234
	v_cvt_pknorm_i16_f32 v9, v230, v231
	v_rcp_f32_e32 v3, v12
	s_mov_b64 s[6:7], 0x2200
	v_cmp_lt_f32_e32 vcc, 0, v12
	v_mov_b32_e32 v26, v44
	v_lshl_add_u64 v[14:15], v[4:5], 0, s[6:7]
	global_store_dwordx4 v[14:15], v[6:9], off sc0 sc1
	s_nop 1
	v_pk_mul_f32 v[6:7], v[10:11], s[4:5] op_sel_hi:[1,0]
	v_cndmask_b32_e32 v3, 0, v3, vcc
	global_store_dwordx2 v0, v[6:7], s[2:3] offset:64
	v_pk_mul_f32 v[224:225], v[26:27], v[2:3] op_sel:[0,1] op_sel_hi:[1,1]
	v_pk_mul_f32 v[226:227], v[28:29], v[2:3] op_sel:[0,1] op_sel_hi:[1,1]
	v_cvt_pknorm_i16_f32 v6, v224, v225
	v_cvt_pknorm_i16_f32 v7, v226, v227
	v_pk_mul_f32 v[228:229], v[30:31], v[2:3] op_sel:[0,1] op_sel_hi:[1,1]
	v_pk_mul_f32 v[230:231], v[32:33], v[2:3] op_sel:[0,1] op_sel_hi:[1,1]
	v_cvt_pknorm_i16_f32 v8, v228, v229
	s_waitcnt lgkmcnt(0)
	v_max_f32_e32 v13, v13, v235
	v_cvt_pknorm_i16_f32 v9, v230, v231
	v_rcp_f32_e32 v3, v13
	v_cmp_lt_f32_e32 vcc, 0, v13
	v_mov_b32_e32 v34, v45
	s_mov_b64 s[6:7], 0x2400
	v_cndmask_b32_e32 v3, 0, v3, vcc
	v_lshl_add_u64 v[10:11], v[4:5], 0, s[6:7]
	global_store_dwordx4 v[10:11], v[6:9], off sc0 sc1
	v_pk_mul_f32 v[224:225], v[34:35], v[2:3] op_sel:[0,1] op_sel_hi:[1,1]
	v_pk_mul_f32 v[226:227], v[36:37], v[2:3] op_sel:[0,1] op_sel_hi:[1,1]
	v_cvt_pknorm_i16_f32 v6, v224, v225
	v_cvt_pknorm_i16_f32 v7, v226, v227
	v_pk_mul_f32 v[228:229], v[38:39], v[2:3] op_sel:[0,1] op_sel_hi:[1,1]
	v_pk_mul_f32 v[230:231], v[40:41], v[2:3] op_sel:[0,1] op_sel_hi:[1,1]
	v_cvt_pknorm_i16_f32 v8, v228, v229
	s_mov_b64 s[6:7], 0x2600
	v_cvt_pknorm_i16_f32 v9, v230, v231
	v_lshl_add_u64 v[10:11], v[4:5], 0, s[6:7]
	global_store_dwordx4 v[10:11], v[6:9], off sc0 sc1
	s_nop 1
	v_pk_mul_f32 v[6:7], v[12:13], s[4:5] op_sel_hi:[1,0]
	v_mov_b64_e32 v[46:47], v[50:51]
	v_mov_b64_e32 v[48:49], v[52:53]
	global_store_dwordx2 v0, v[6:7], s[2:3] offset:72
	v_mov_b64_e32 v[32:33], v[46:47]
	v_accvgpr_read_b32 v6, a28
	v_accvgpr_read_b32 v7, a44
	v_max3_f32 v8, |v32|, |v6|, |v7|
	v_accvgpr_read_b32 v9, a60
	v_accvgpr_read_b32 v14, a76
	v_max3_f32 v8, |v8|, |v9|, |v14|
	v_accvgpr_read_b32 v15, a124
	v_accvgpr_read_b32 v16, a140
	v_max3_f32 v8, |v8|, |v15|, |v16|
	v_accvgpr_read_b32 v10, a92
	v_accvgpr_read_b32 v17, a92
	v_max3_f32 v8, |v8|, |v17|, |v10|
	v_accvgpr_read_b32 v19, a29
	v_accvgpr_read_b32 v20, a45
	v_max3_f32 v10, |v33|, |v19|, |v20|
	v_accvgpr_read_b32 v21, a61
	v_accvgpr_read_b32 v22, a77
	v_max3_f32 v10, |v10|, |v21|, |v22|
	v_accvgpr_read_b32 v23, a125
	v_accvgpr_read_b32 v24, a141
	v_max3_f32 v10, |v10|, |v23|, |v24|
	v_mov_b64_e32 v[34:35], v[48:49]
	v_accvgpr_read_b32 v25, a93
	v_max3_f32 v11, |v10|, |v25|, |v25|
	v_accvgpr_read_b32 v27, a30
	v_accvgpr_read_b32 v28, a46
	v_max3_f32 v10, |v34|, |v27|, |v28|
	v_accvgpr_read_b32 v29, a62
	v_accvgpr_read_b32 v30, a78
	v_max3_f32 v10, |v10|, |v29|, |v30|
	v_mov_b32_e32 v3, v32
	v_accvgpr_read_b32 v31, a126
	v_accvgpr_read_b32 v32, a142
	v_max3_f32 v10, |v10|, |v31|, |v32|
	v_mov_b32_e32 v18, v33
	v_mov_b32_e32 v26, v34
	v_accvgpr_read_b32 v33, a94
	v_max3_f32 v12, |v10|, |v33|, |v33|
	v_mov_b32_e32 v34, v35
	v_accvgpr_read_b32 v35, a31
	v_accvgpr_read_b32 v36, a47
	v_max3_f32 v10, |v34|, |v35|, |v36|
	v_accvgpr_read_b32 v37, a63
	v_accvgpr_read_b32 v38, a79
	v_max3_f32 v10, |v10|, |v37|, |v38|
	v_accvgpr_read_b32 v39, a127
	v_accvgpr_read_b32 v40, a143
	v_max3_f32 v10, |v10|, |v39|, |v40|
	v_accvgpr_read_b32 v41, a95
	v_max3_f32 v13, |v10|, |v41|, |v41|
	s_mov_b64 s[6:7], 0x3000
	s_nop 1
	v_max_f32_dpp v8, v8, v8 quad_perm:[1,0,3,2] row_mask:0xf bank_mask:0xf
	v_max_f32_dpp v11, v11, v11 quad_perm:[1,0,3,2] row_mask:0xf bank_mask:0xf
	v_max_f32_dpp v12, v12, v12 quad_perm:[1,0,3,2] row_mask:0xf bank_mask:0xf
	v_max_f32_dpp v13, v13, v13 quad_perm:[1,0,3,2] row_mask:0xf bank_mask:0xf
	v_max_f32_dpp v8, v8, v8 quad_perm:[2,3,0,1] row_mask:0xf bank_mask:0xf
	v_max_f32_dpp v11, v11, v11 quad_perm:[2,3,0,1] row_mask:0xf bank_mask:0xf
	v_max_f32_dpp v12, v12, v12 quad_perm:[2,3,0,1] row_mask:0xf bank_mask:0xf
	v_max_f32_dpp v13, v13, v13 quad_perm:[2,3,0,1] row_mask:0xf bank_mask:0xf
	v_max_f32_dpp v8, v8, v8 row_half_mirror row_mask:0xf bank_mask:0xf
	v_max_f32_dpp v11, v11, v11 row_half_mirror row_mask:0xf bank_mask:0xf
	v_max_f32_dpp v12, v12, v12 row_half_mirror row_mask:0xf bank_mask:0xf
	v_max_f32_dpp v13, v13, v13 row_half_mirror row_mask:0xf bank_mask:0xf
	v_max_f32_dpp v8, v8, v8 row_mirror row_mask:0xf bank_mask:0xf
	v_max_f32_dpp v11, v11, v11 row_mirror row_mask:0xf bank_mask:0xf
	v_max_f32_dpp v12, v12, v12 row_mirror row_mask:0xf bank_mask:0xf
	v_max_f32_dpp v13, v13, v13 row_mirror row_mask:0xf bank_mask:0xf
	s_nop 0
	ds_swizzle_b32 v232, v8 offset:swizzle(SWAP,16)
	ds_swizzle_b32 v233, v11 offset:swizzle(SWAP,16)
	ds_swizzle_b32 v234, v12 offset:swizzle(SWAP,16)
	ds_swizzle_b32 v235, v13 offset:swizzle(SWAP,16)
	s_waitcnt lgkmcnt(0)
	v_max_f32_e32 v10, v8, v232
	v_rcp_f32_e32 v8, v10
	v_cmp_lt_f32_e32 vcc, 0, v10
	s_waitcnt lgkmcnt(0)
	v_max_f32_e32 v11, v11, v233
	s_waitcnt lgkmcnt(0)
	v_max_f32_e32 v12, v12, v234
	v_cndmask_b32_e32 v42, 0, v8, vcc
	v_mul_f32_e32 v3, v42, v3
	v_mul_f32_e32 v6, v42, v6
	v_cvt_pknorm_i16_f32 v6, v3, v6
	v_mul_f32_e32 v3, v42, v7
	v_mul_f32_e32 v7, v42, v9
	v_cvt_pknorm_i16_f32 v7, v3, v7
	v_pk_mul_f32 v[224:225], v[14:15], v[42:43] op_sel_hi:[1,0]
	v_pk_mul_f32 v[226:227], v[16:17], v[42:43] op_sel_hi:[1,0]
	v_cvt_pknorm_i16_f32 v8, v224, v225
	v_cvt_pknorm_i16_f32 v9, v226, v227
	v_rcp_f32_e32 v3, v11
	v_cmp_lt_f32_e32 vcc, 0, v11
	v_lshl_add_u64 v[14:15], v[4:5], 0, s[6:7]
	global_store_dwordx4 v[14:15], v[6:9], off sc0 sc1
	s_mov_b64 s[6:7], 0x3200
	v_cndmask_b32_e32 v3, 0, v3, vcc
	v_pk_mul_f32 v[228:229], v[18:19], v[2:3] op_sel:[0,1] op_sel_hi:[1,1]
	v_pk_mul_f32 v[230:231], v[20:21], v[2:3] op_sel:[0,1] op_sel_hi:[1,1]
	v_cvt_pknorm_i16_f32 v6, v228, v229
	v_cvt_pknorm_i16_f32 v7, v230, v231
	v_pk_mul_f32 v[224:225], v[22:23], v[2:3] op_sel:[0,1] op_sel_hi:[1,1]
	v_pk_mul_f32 v[226:227], v[24:25], v[2:3] op_sel:[0,1] op_sel_hi:[1,1]
	v_cvt_pknorm_i16_f32 v8, v224, v225
	v_cvt_pknorm_i16_f32 v9, v226, v227
	v_rcp_f32_e32 v3, v12
	v_cmp_lt_f32_e32 vcc, 0, v12
	v_lshl_add_u64 v[14:15], v[4:5], 0, s[6:7]
	global_store_dwordx4 v[14:15], v[6:9], off sc0 sc1
	s_nop 1
	v_pk_mul_f32 v[6:7], v[10:11], s[4:5] op_sel_hi:[1,0]
	v_cndmask_b32_e32 v3, 0, v3, vcc
	global_store_dwordx2 v0, v[6:7], s[2:3] offset:96
	v_pk_mul_f32 v[228:229], v[26:27], v[2:3] op_sel:[0,1] op_sel_hi:[1,1]
	v_pk_mul_f32 v[230:231], v[28:29], v[2:3] op_sel:[0,1] op_sel_hi:[1,1]
	v_cvt_pknorm_i16_f32 v6, v228, v229
	v_cvt_pknorm_i16_f32 v7, v230, v231
	v_pk_mul_f32 v[224:225], v[30:31], v[2:3] op_sel:[0,1] op_sel_hi:[1,1]
	v_pk_mul_f32 v[226:227], v[32:33], v[2:3] op_sel:[0,1] op_sel_hi:[1,1]
	v_cvt_pknorm_i16_f32 v8, v224, v225
	s_waitcnt lgkmcnt(0)
	v_max_f32_e32 v13, v13, v235
	v_cvt_pknorm_i16_f32 v9, v226, v227
	v_rcp_f32_e32 v3, v13
	v_cmp_lt_f32_e32 vcc, 0, v13
	s_mov_b64 s[6:7], 0x3400
	v_lshl_add_u64 v[10:11], v[4:5], 0, s[6:7]
	v_cndmask_b32_e32 v3, 0, v3, vcc
	global_store_dwordx4 v[10:11], v[6:9], off sc0 sc1
	v_pk_mul_f32 v[228:229], v[34:35], v[2:3] op_sel:[0,1] op_sel_hi:[1,1]
	v_pk_mul_f32 v[230:231], v[36:37], v[2:3] op_sel:[0,1] op_sel_hi:[1,1]
	v_cvt_pknorm_i16_f32 v6, v228, v229
	v_cvt_pknorm_i16_f32 v7, v230, v231
	v_pk_mul_f32 v[224:225], v[38:39], v[2:3] op_sel:[0,1] op_sel_hi:[1,1]
	v_pk_mul_f32 v[226:227], v[40:41], v[2:3] op_sel:[0,1] op_sel_hi:[1,1]
	v_cvt_pknorm_i16_f32 v8, v224, v225
	s_mov_b64 s[6:7], 0x3600
	v_cvt_pknorm_i16_f32 v9, v226, v227
	v_lshl_add_u64 v[10:11], v[4:5], 0, s[6:7]
	global_store_dwordx4 v[10:11], v[6:9], off sc0 sc1
	s_nop 1
	v_pk_mul_f32 v[6:7], v[12:13], s[4:5] op_sel_hi:[1,0]
	global_store_dwordx2 v0, v[6:7], s[2:3] offset:104
	v_accvgpr_read_b32 v3, a240
	v_accvgpr_read_b32 v6, a224
	v_accvgpr_read_b32 v7, a208
	v_max3_f32 v8, |v3|, |v6|, |v7|
	v_accvgpr_read_b32 v9, a192
	v_accvgpr_read_b32 v14, a176
	v_max3_f32 v8, |v8|, |v9|, |v14|
	v_accvgpr_read_b32 v15, a160
	v_accvgpr_read_b32 v16, a144
	v_max3_f32 v8, |v8|, |v15|, |v16|
	v_accvgpr_read_b32 v10, a96
	v_accvgpr_read_b32 v17, a96
	v_max3_f32 v8, |v8|, |v17|, |v10|
	v_accvgpr_read_b32 v18, a241
	v_accvgpr_read_b32 v19, a225
	v_accvgpr_read_b32 v20, a209
	v_max3_f32 v10, |v18|, |v19|, |v20|
	v_accvgpr_read_b32 v21, a193
	v_accvgpr_read_b32 v22, a177
	v_max3_f32 v10, |v10|, |v21|, |v22|
	v_accvgpr_read_b32 v23, a161
	v_accvgpr_read_b32 v24, a145
	v_max3_f32 v10, |v10|, |v23|, |v24|
	v_accvgpr_read_b32 v25, a97
	v_max3_f32 v11, |v10|, |v25|, |v25|
	v_accvgpr_read_b32 v26, a242
	v_accvgpr_read_b32 v27, a226
	v_accvgpr_read_b32 v28, a210
	v_max3_f32 v10, |v26|, |v27|, |v28|
	v_accvgpr_read_b32 v29, a194
	v_accvgpr_read_b32 v30, a178
	v_max3_f32 v10, |v10|, |v29|, |v30|
	v_accvgpr_read_b32 v31, a162
	v_accvgpr_read_b32 v32, a146
	v_max3_f32 v10, |v10|, |v31|, |v32|
	v_accvgpr_read_b32 v33, a98
	v_max3_f32 v12, |v10|, |v33|, |v33|
	v_accvgpr_read_b32 v34, a243
	v_accvgpr_read_b32 v35, a227
	v_accvgpr_read_b32 v36, a211
	v_max3_f32 v10, |v34|, |v35|, |v36|
	v_accvgpr_read_b32 v37, a195
	v_accvgpr_read_b32 v38, a179
	v_max3_f32 v10, |v10|, |v37|, |v38|
	v_accvgpr_read_b32 v39, a163
	v_accvgpr_read_b32 v40, a147
	v_max3_f32 v10, |v10|, |v39|, |v40|
	v_accvgpr_read_b32 v41, a99
	v_max3_f32 v13, |v10|, |v41|, |v41|
	s_mov_b64 s[6:7], 0x4000
	s_nop 1
	v_max_f32_dpp v8, v8, v8 quad_perm:[1,0,3,2] row_mask:0xf bank_mask:0xf
	v_max_f32_dpp v11, v11, v11 quad_perm:[1,0,3,2] row_mask:0xf bank_mask:0xf
	v_max_f32_dpp v12, v12, v12 quad_perm:[1,0,3,2] row_mask:0xf bank_mask:0xf
	v_max_f32_dpp v13, v13, v13 quad_perm:[1,0,3,2] row_mask:0xf bank_mask:0xf
	v_max_f32_dpp v8, v8, v8 quad_perm:[2,3,0,1] row_mask:0xf bank_mask:0xf
	v_max_f32_dpp v11, v11, v11 quad_perm:[2,3,0,1] row_mask:0xf bank_mask:0xf
	v_max_f32_dpp v12, v12, v12 quad_perm:[2,3,0,1] row_mask:0xf bank_mask:0xf
	v_max_f32_dpp v13, v13, v13 quad_perm:[2,3,0,1] row_mask:0xf bank_mask:0xf
	v_max_f32_dpp v8, v8, v8 row_half_mirror row_mask:0xf bank_mask:0xf
	v_max_f32_dpp v11, v11, v11 row_half_mirror row_mask:0xf bank_mask:0xf
	v_max_f32_dpp v12, v12, v12 row_half_mirror row_mask:0xf bank_mask:0xf
	v_max_f32_dpp v13, v13, v13 row_half_mirror row_mask:0xf bank_mask:0xf
	v_max_f32_dpp v8, v8, v8 row_mirror row_mask:0xf bank_mask:0xf
	v_max_f32_dpp v11, v11, v11 row_mirror row_mask:0xf bank_mask:0xf
	v_max_f32_dpp v12, v12, v12 row_mirror row_mask:0xf bank_mask:0xf
	v_max_f32_dpp v13, v13, v13 row_mirror row_mask:0xf bank_mask:0xf
	s_nop 0
	ds_swizzle_b32 v232, v8 offset:swizzle(SWAP,16)
	ds_swizzle_b32 v233, v11 offset:swizzle(SWAP,16)
	ds_swizzle_b32 v234, v12 offset:swizzle(SWAP,16)
	ds_swizzle_b32 v235, v13 offset:swizzle(SWAP,16)
	s_waitcnt lgkmcnt(0)
	v_max_f32_e32 v10, v8, v232
	v_rcp_f32_e32 v8, v10
	v_cmp_lt_f32_e32 vcc, 0, v10
	s_waitcnt lgkmcnt(0)
	v_max_f32_e32 v11, v11, v233
	s_waitcnt lgkmcnt(0)
	v_max_f32_e32 v12, v12, v234
	v_cndmask_b32_e32 v42, 0, v8, vcc
	v_mul_f32_e32 v3, v42, v3
	v_mul_f32_e32 v6, v42, v6
	v_cvt_pknorm_i16_f32 v6, v3, v6
	v_mul_f32_e32 v3, v42, v7
	v_mul_f32_e32 v7, v42, v9
	v_cvt_pknorm_i16_f32 v7, v3, v7
	v_pk_mul_f32 v[228:229], v[14:15], v[42:43] op_sel_hi:[1,0]
	v_pk_mul_f32 v[230:231], v[16:17], v[42:43] op_sel_hi:[1,0]
	v_cvt_pknorm_i16_f32 v8, v228, v229
	v_cvt_pknorm_i16_f32 v9, v230, v231
	v_rcp_f32_e32 v3, v11
	v_cmp_lt_f32_e32 vcc, 0, v11
	v_lshl_add_u64 v[14:15], v[4:5], 0, s[6:7]
	global_store_dwordx4 v[14:15], v[6:9], off sc0 sc1
	s_mov_b64 s[6:7], 0x4200
	v_cndmask_b32_e32 v3, 0, v3, vcc
	v_pk_mul_f32 v[224:225], v[18:19], v[2:3] op_sel:[0,1] op_sel_hi:[1,1]
	v_pk_mul_f32 v[226:227], v[20:21], v[2:3] op_sel:[0,1] op_sel_hi:[1,1]
	v_cvt_pknorm_i16_f32 v6, v224, v225
	v_cvt_pknorm_i16_f32 v7, v226, v227
	v_pk_mul_f32 v[228:229], v[22:23], v[2:3] op_sel:[0,1] op_sel_hi:[1,1]
	v_pk_mul_f32 v[230:231], v[24:25], v[2:3] op_sel:[0,1] op_sel_hi:[1,1]
	v_cvt_pknorm_i16_f32 v8, v228, v229
	v_cvt_pknorm_i16_f32 v9, v230, v231
	v_rcp_f32_e32 v3, v12
	v_cmp_lt_f32_e32 vcc, 0, v12
	v_lshl_add_u64 v[14:15], v[4:5], 0, s[6:7]
	global_store_dwordx4 v[14:15], v[6:9], off sc0 sc1
	s_nop 1
	v_pk_mul_f32 v[6:7], v[10:11], s[4:5] op_sel_hi:[1,0]
	v_cndmask_b32_e32 v3, 0, v3, vcc
	global_store_dwordx2 v0, v[6:7], s[2:3] offset:128
	v_pk_mul_f32 v[224:225], v[26:27], v[2:3] op_sel:[0,1] op_sel_hi:[1,1]
	v_pk_mul_f32 v[226:227], v[28:29], v[2:3] op_sel:[0,1] op_sel_hi:[1,1]
	v_cvt_pknorm_i16_f32 v6, v224, v225
	v_cvt_pknorm_i16_f32 v7, v226, v227
	v_pk_mul_f32 v[228:229], v[30:31], v[2:3] op_sel:[0,1] op_sel_hi:[1,1]
	v_pk_mul_f32 v[230:231], v[32:33], v[2:3] op_sel:[0,1] op_sel_hi:[1,1]
	v_cvt_pknorm_i16_f32 v8, v228, v229
	s_waitcnt lgkmcnt(0)
	v_max_f32_e32 v13, v13, v235
	v_cvt_pknorm_i16_f32 v9, v230, v231
	v_rcp_f32_e32 v3, v13
	v_cmp_lt_f32_e32 vcc, 0, v13
	s_mov_b64 s[6:7], 0x4400
	v_lshl_add_u64 v[10:11], v[4:5], 0, s[6:7]
	v_cndmask_b32_e32 v3, 0, v3, vcc
	global_store_dwordx4 v[10:11], v[6:9], off sc0 sc1
	v_pk_mul_f32 v[224:225], v[34:35], v[2:3] op_sel:[0,1] op_sel_hi:[1,1]
	v_pk_mul_f32 v[226:227], v[36:37], v[2:3] op_sel:[0,1] op_sel_hi:[1,1]
	v_cvt_pknorm_i16_f32 v6, v224, v225
	v_cvt_pknorm_i16_f32 v7, v226, v227
	v_pk_mul_f32 v[228:229], v[38:39], v[2:3] op_sel:[0,1] op_sel_hi:[1,1]
	v_pk_mul_f32 v[230:231], v[40:41], v[2:3] op_sel:[0,1] op_sel_hi:[1,1]
	v_cvt_pknorm_i16_f32 v8, v228, v229
	s_mov_b64 s[6:7], 0x4600
	v_cvt_pknorm_i16_f32 v9, v230, v231
	v_lshl_add_u64 v[10:11], v[4:5], 0, s[6:7]
	global_store_dwordx4 v[10:11], v[6:9], off sc0 sc1
	s_nop 1
	v_pk_mul_f32 v[6:7], v[12:13], s[4:5] op_sel_hi:[1,0]
	global_store_dwordx2 v0, v[6:7], s[2:3] offset:136
	v_accvgpr_read_b32 v3, a244
	v_accvgpr_read_b32 v6, a228
	v_accvgpr_read_b32 v7, a212
	v_max3_f32 v8, |v3|, |v6|, |v7|
	v_accvgpr_read_b32 v9, a196
	v_accvgpr_read_b32 v14, a180
	v_max3_f32 v8, |v8|, |v9|, |v14|
	v_accvgpr_read_b32 v15, a164
	v_accvgpr_read_b32 v16, a148
	v_max3_f32 v8, |v8|, |v15|, |v16|
	v_accvgpr_read_b32 v10, a100
	v_accvgpr_read_b32 v17, a100
	v_max3_f32 v8, |v8|, |v17|, |v10|
	v_accvgpr_read_b32 v18, a245
	v_accvgpr_read_b32 v19, a229
	v_accvgpr_read_b32 v20, a213
	v_max3_f32 v10, |v18|, |v19|, |v20|
	v_accvgpr_read_b32 v21, a197
	v_accvgpr_read_b32 v22, a181
	v_max3_f32 v10, |v10|, |v21|, |v22|
	v_accvgpr_read_b32 v23, a165
	v_accvgpr_read_b32 v24, a149
	v_max3_f32 v10, |v10|, |v23|, |v24|
	v_accvgpr_read_b32 v25, a101
	v_max3_f32 v11, |v10|, |v25|, |v25|
	v_accvgpr_read_b32 v26, a246
	v_accvgpr_read_b32 v27, a230
	v_accvgpr_read_b32 v28, a214
	v_max3_f32 v10, |v26|, |v27|, |v28|
	v_accvgpr_read_b32 v29, a198
	v_accvgpr_read_b32 v30, a182
	v_max3_f32 v10, |v10|, |v29|, |v30|
	v_accvgpr_read_b32 v31, a166
	v_accvgpr_read_b32 v32, a150
	v_max3_f32 v10, |v10|, |v31|, |v32|
	v_accvgpr_read_b32 v33, a102
	v_max3_f32 v12, |v10|, |v33|, |v33|
	v_accvgpr_read_b32 v34, a247
	v_accvgpr_read_b32 v35, a231
	v_accvgpr_read_b32 v36, a215
	v_max3_f32 v10, |v34|, |v35|, |v36|
	v_accvgpr_read_b32 v37, a199
	v_accvgpr_read_b32 v38, a183
	v_max3_f32 v10, |v10|, |v37|, |v38|
	v_accvgpr_read_b32 v39, a167
	v_accvgpr_read_b32 v40, a151
	v_max3_f32 v10, |v10|, |v39|, |v40|
	v_accvgpr_read_b32 v41, a103
	v_max3_f32 v13, |v10|, |v41|, |v41|
	s_mov_b64 s[6:7], 0x5000
	s_nop 1
	v_max_f32_dpp v8, v8, v8 quad_perm:[1,0,3,2] row_mask:0xf bank_mask:0xf
	v_max_f32_dpp v11, v11, v11 quad_perm:[1,0,3,2] row_mask:0xf bank_mask:0xf
	v_max_f32_dpp v12, v12, v12 quad_perm:[1,0,3,2] row_mask:0xf bank_mask:0xf
	v_max_f32_dpp v13, v13, v13 quad_perm:[1,0,3,2] row_mask:0xf bank_mask:0xf
	v_max_f32_dpp v8, v8, v8 quad_perm:[2,3,0,1] row_mask:0xf bank_mask:0xf
	v_max_f32_dpp v11, v11, v11 quad_perm:[2,3,0,1] row_mask:0xf bank_mask:0xf
	v_max_f32_dpp v12, v12, v12 quad_perm:[2,3,0,1] row_mask:0xf bank_mask:0xf
	v_max_f32_dpp v13, v13, v13 quad_perm:[2,3,0,1] row_mask:0xf bank_mask:0xf
	v_max_f32_dpp v8, v8, v8 row_half_mirror row_mask:0xf bank_mask:0xf
	v_max_f32_dpp v11, v11, v11 row_half_mirror row_mask:0xf bank_mask:0xf
	v_max_f32_dpp v12, v12, v12 row_half_mirror row_mask:0xf bank_mask:0xf
	v_max_f32_dpp v13, v13, v13 row_half_mirror row_mask:0xf bank_mask:0xf
	v_max_f32_dpp v8, v8, v8 row_mirror row_mask:0xf bank_mask:0xf
	v_max_f32_dpp v11, v11, v11 row_mirror row_mask:0xf bank_mask:0xf
	v_max_f32_dpp v12, v12, v12 row_mirror row_mask:0xf bank_mask:0xf
	v_max_f32_dpp v13, v13, v13 row_mirror row_mask:0xf bank_mask:0xf
	s_nop 0
	ds_swizzle_b32 v232, v8 offset:swizzle(SWAP,16)
	ds_swizzle_b32 v233, v11 offset:swizzle(SWAP,16)
	ds_swizzle_b32 v234, v12 offset:swizzle(SWAP,16)
	ds_swizzle_b32 v235, v13 offset:swizzle(SWAP,16)
	s_waitcnt lgkmcnt(0)
	v_max_f32_e32 v10, v8, v232
	v_rcp_f32_e32 v8, v10
	v_cmp_lt_f32_e32 vcc, 0, v10
	s_waitcnt lgkmcnt(0)
	v_max_f32_e32 v11, v11, v233
	s_waitcnt lgkmcnt(0)
	v_max_f32_e32 v12, v12, v234
	v_cndmask_b32_e32 v42, 0, v8, vcc
	v_mul_f32_e32 v3, v42, v3
	v_mul_f32_e32 v6, v42, v6
	v_cvt_pknorm_i16_f32 v6, v3, v6
	v_mul_f32_e32 v3, v42, v7
	v_mul_f32_e32 v7, v42, v9
	v_cvt_pknorm_i16_f32 v7, v3, v7
	v_pk_mul_f32 v[224:225], v[14:15], v[42:43] op_sel_hi:[1,0]
	v_pk_mul_f32 v[226:227], v[16:17], v[42:43] op_sel_hi:[1,0]
	v_cvt_pknorm_i16_f32 v8, v224, v225
	v_cvt_pknorm_i16_f32 v9, v226, v227
	v_rcp_f32_e32 v3, v11
	v_cmp_lt_f32_e32 vcc, 0, v11
	v_lshl_add_u64 v[14:15], v[4:5], 0, s[6:7]
	global_store_dwordx4 v[14:15], v[6:9], off sc0 sc1
	s_mov_b64 s[6:7], 0x5200
	v_cndmask_b32_e32 v3, 0, v3, vcc
	v_pk_mul_f32 v[228:229], v[18:19], v[2:3] op_sel:[0,1] op_sel_hi:[1,1]
	v_pk_mul_f32 v[230:231], v[20:21], v[2:3] op_sel:[0,1] op_sel_hi:[1,1]
	v_cvt_pknorm_i16_f32 v6, v228, v229
	v_cvt_pknorm_i16_f32 v7, v230, v231
	v_pk_mul_f32 v[224:225], v[22:23], v[2:3] op_sel:[0,1] op_sel_hi:[1,1]
	v_pk_mul_f32 v[226:227], v[24:25], v[2:3] op_sel:[0,1] op_sel_hi:[1,1]
	v_cvt_pknorm_i16_f32 v8, v224, v225
	v_cvt_pknorm_i16_f32 v9, v226, v227
	v_rcp_f32_e32 v3, v12
	v_cmp_lt_f32_e32 vcc, 0, v12
	v_lshl_add_u64 v[14:15], v[4:5], 0, s[6:7]
	global_store_dwordx4 v[14:15], v[6:9], off sc0 sc1
	s_nop 1
	v_pk_mul_f32 v[6:7], v[10:11], s[4:5] op_sel_hi:[1,0]
	v_cndmask_b32_e32 v3, 0, v3, vcc
	global_store_dwordx2 v0, v[6:7], s[2:3] offset:160
	v_pk_mul_f32 v[228:229], v[26:27], v[2:3] op_sel:[0,1] op_sel_hi:[1,1]
	v_pk_mul_f32 v[230:231], v[28:29], v[2:3] op_sel:[0,1] op_sel_hi:[1,1]
	v_cvt_pknorm_i16_f32 v6, v228, v229
	v_cvt_pknorm_i16_f32 v7, v230, v231
	v_pk_mul_f32 v[224:225], v[30:31], v[2:3] op_sel:[0,1] op_sel_hi:[1,1]
	v_pk_mul_f32 v[226:227], v[32:33], v[2:3] op_sel:[0,1] op_sel_hi:[1,1]
	v_cvt_pknorm_i16_f32 v8, v224, v225
	s_waitcnt lgkmcnt(0)
	v_max_f32_e32 v13, v13, v235
	v_cvt_pknorm_i16_f32 v9, v226, v227
	v_rcp_f32_e32 v3, v13
	v_cmp_lt_f32_e32 vcc, 0, v13
	s_mov_b64 s[6:7], 0x5400
	v_lshl_add_u64 v[10:11], v[4:5], 0, s[6:7]
	v_cndmask_b32_e32 v3, 0, v3, vcc
	global_store_dwordx4 v[10:11], v[6:9], off sc0 sc1
	v_pk_mul_f32 v[228:229], v[34:35], v[2:3] op_sel:[0,1] op_sel_hi:[1,1]
	v_pk_mul_f32 v[230:231], v[36:37], v[2:3] op_sel:[0,1] op_sel_hi:[1,1]
	v_cvt_pknorm_i16_f32 v6, v228, v229
	v_cvt_pknorm_i16_f32 v7, v230, v231
	v_pk_mul_f32 v[224:225], v[38:39], v[2:3] op_sel:[0,1] op_sel_hi:[1,1]
	v_pk_mul_f32 v[226:227], v[40:41], v[2:3] op_sel:[0,1] op_sel_hi:[1,1]
	v_cvt_pknorm_i16_f32 v8, v224, v225
	s_mov_b64 s[6:7], 0x5600
	v_cvt_pknorm_i16_f32 v9, v226, v227
	v_lshl_add_u64 v[10:11], v[4:5], 0, s[6:7]
	global_store_dwordx4 v[10:11], v[6:9], off sc0 sc1
	s_nop 1
	v_pk_mul_f32 v[6:7], v[12:13], s[4:5] op_sel_hi:[1,0]
	global_store_dwordx2 v0, v[6:7], s[2:3] offset:168
	v_accvgpr_read_b32 v3, a248
	v_accvgpr_read_b32 v6, a232
	v_accvgpr_read_b32 v7, a216
	v_max3_f32 v8, |v3|, |v6|, |v7|
	v_accvgpr_read_b32 v9, a200
	v_accvgpr_read_b32 v14, a184
	v_max3_f32 v8, |v8|, |v9|, |v14|
	v_accvgpr_read_b32 v15, a168
	v_accvgpr_read_b32 v16, a152
	v_max3_f32 v8, |v8|, |v15|, |v16|
	v_accvgpr_read_b32 v10, a104
	v_accvgpr_read_b32 v17, a104
	v_max3_f32 v8, |v8|, |v17|, |v10|
	v_accvgpr_read_b32 v18, a249
	v_accvgpr_read_b32 v19, a233
	v_accvgpr_read_b32 v20, a217
	v_max3_f32 v10, |v18|, |v19|, |v20|
	v_accvgpr_read_b32 v21, a201
	v_accvgpr_read_b32 v22, a185
	v_max3_f32 v10, |v10|, |v21|, |v22|
	v_accvgpr_read_b32 v23, a169
	v_accvgpr_read_b32 v24, a153
	v_max3_f32 v10, |v10|, |v23|, |v24|
	v_accvgpr_read_b32 v25, a105
	v_max3_f32 v11, |v10|, |v25|, |v25|
	v_accvgpr_read_b32 v26, a250
	v_accvgpr_read_b32 v27, a234
	v_accvgpr_read_b32 v28, a218
	v_max3_f32 v10, |v26|, |v27|, |v28|
	v_accvgpr_read_b32 v29, a202
	v_accvgpr_read_b32 v30, a186
	v_max3_f32 v10, |v10|, |v29|, |v30|
	v_accvgpr_read_b32 v31, a170
	v_accvgpr_read_b32 v32, a154
	v_max3_f32 v10, |v10|, |v31|, |v32|
	v_accvgpr_read_b32 v33, a106
	v_max3_f32 v12, |v10|, |v33|, |v33|
	v_accvgpr_read_b32 v34, a251
	v_accvgpr_read_b32 v35, a235
	v_accvgpr_read_b32 v36, a219
	v_max3_f32 v10, |v34|, |v35|, |v36|
	v_accvgpr_read_b32 v37, a203
	v_accvgpr_read_b32 v38, a187
	v_max3_f32 v10, |v10|, |v37|, |v38|
	v_accvgpr_read_b32 v39, a171
	v_accvgpr_read_b32 v40, a155
	v_max3_f32 v10, |v10|, |v39|, |v40|
	v_accvgpr_read_b32 v41, a107
	v_max3_f32 v13, |v10|, |v41|, |v41|
	s_mov_b64 s[6:7], 0x6000
	s_nop 1
	v_max_f32_dpp v8, v8, v8 quad_perm:[1,0,3,2] row_mask:0xf bank_mask:0xf
	v_max_f32_dpp v11, v11, v11 quad_perm:[1,0,3,2] row_mask:0xf bank_mask:0xf
	v_max_f32_dpp v12, v12, v12 quad_perm:[1,0,3,2] row_mask:0xf bank_mask:0xf
	v_max_f32_dpp v13, v13, v13 quad_perm:[1,0,3,2] row_mask:0xf bank_mask:0xf
	v_max_f32_dpp v8, v8, v8 quad_perm:[2,3,0,1] row_mask:0xf bank_mask:0xf
	v_max_f32_dpp v11, v11, v11 quad_perm:[2,3,0,1] row_mask:0xf bank_mask:0xf
	v_max_f32_dpp v12, v12, v12 quad_perm:[2,3,0,1] row_mask:0xf bank_mask:0xf
	v_max_f32_dpp v13, v13, v13 quad_perm:[2,3,0,1] row_mask:0xf bank_mask:0xf
	v_max_f32_dpp v8, v8, v8 row_half_mirror row_mask:0xf bank_mask:0xf
	v_max_f32_dpp v11, v11, v11 row_half_mirror row_mask:0xf bank_mask:0xf
	v_max_f32_dpp v12, v12, v12 row_half_mirror row_mask:0xf bank_mask:0xf
	v_max_f32_dpp v13, v13, v13 row_half_mirror row_mask:0xf bank_mask:0xf
	v_max_f32_dpp v8, v8, v8 row_mirror row_mask:0xf bank_mask:0xf
	v_max_f32_dpp v11, v11, v11 row_mirror row_mask:0xf bank_mask:0xf
	v_max_f32_dpp v12, v12, v12 row_mirror row_mask:0xf bank_mask:0xf
	v_max_f32_dpp v13, v13, v13 row_mirror row_mask:0xf bank_mask:0xf
	s_nop 0
	ds_swizzle_b32 v232, v8 offset:swizzle(SWAP,16)
	ds_swizzle_b32 v233, v11 offset:swizzle(SWAP,16)
	ds_swizzle_b32 v234, v12 offset:swizzle(SWAP,16)
	ds_swizzle_b32 v235, v13 offset:swizzle(SWAP,16)
	s_waitcnt lgkmcnt(0)
	v_max_f32_e32 v10, v8, v232
	v_rcp_f32_e32 v8, v10
	v_cmp_lt_f32_e32 vcc, 0, v10
	s_waitcnt lgkmcnt(0)
	v_max_f32_e32 v11, v11, v233
	s_waitcnt lgkmcnt(0)
	v_max_f32_e32 v12, v12, v234
	v_cndmask_b32_e32 v42, 0, v8, vcc
	v_mul_f32_e32 v3, v42, v3
	v_mul_f32_e32 v6, v42, v6
	v_cvt_pknorm_i16_f32 v6, v3, v6
	v_mul_f32_e32 v3, v42, v7
	v_mul_f32_e32 v7, v42, v9
	v_cvt_pknorm_i16_f32 v7, v3, v7
	v_pk_mul_f32 v[228:229], v[14:15], v[42:43] op_sel_hi:[1,0]
	v_pk_mul_f32 v[230:231], v[16:17], v[42:43] op_sel_hi:[1,0]
	v_cvt_pknorm_i16_f32 v8, v228, v229
	v_cvt_pknorm_i16_f32 v9, v230, v231
	v_rcp_f32_e32 v3, v11
	v_cmp_lt_f32_e32 vcc, 0, v11
	v_lshl_add_u64 v[14:15], v[4:5], 0, s[6:7]
	global_store_dwordx4 v[14:15], v[6:9], off sc0 sc1
	s_mov_b64 s[6:7], 0x6200
	v_cndmask_b32_e32 v3, 0, v3, vcc
	v_pk_mul_f32 v[224:225], v[18:19], v[2:3] op_sel:[0,1] op_sel_hi:[1,1]
	v_pk_mul_f32 v[226:227], v[20:21], v[2:3] op_sel:[0,1] op_sel_hi:[1,1]
	v_cvt_pknorm_i16_f32 v6, v224, v225
	v_cvt_pknorm_i16_f32 v7, v226, v227
	v_pk_mul_f32 v[228:229], v[22:23], v[2:3] op_sel:[0,1] op_sel_hi:[1,1]
	v_pk_mul_f32 v[230:231], v[24:25], v[2:3] op_sel:[0,1] op_sel_hi:[1,1]
	v_cvt_pknorm_i16_f32 v8, v228, v229
	v_cvt_pknorm_i16_f32 v9, v230, v231
	v_rcp_f32_e32 v3, v12
	v_cmp_lt_f32_e32 vcc, 0, v12
	v_lshl_add_u64 v[14:15], v[4:5], 0, s[6:7]
	global_store_dwordx4 v[14:15], v[6:9], off sc0 sc1
	s_nop 1
	v_pk_mul_f32 v[6:7], v[10:11], s[4:5] op_sel_hi:[1,0]
	v_cndmask_b32_e32 v3, 0, v3, vcc
	global_store_dwordx2 v0, v[6:7], s[2:3] offset:192
	v_pk_mul_f32 v[224:225], v[26:27], v[2:3] op_sel:[0,1] op_sel_hi:[1,1]
	v_pk_mul_f32 v[226:227], v[28:29], v[2:3] op_sel:[0,1] op_sel_hi:[1,1]
	v_cvt_pknorm_i16_f32 v6, v224, v225
	v_cvt_pknorm_i16_f32 v7, v226, v227
	v_pk_mul_f32 v[228:229], v[30:31], v[2:3] op_sel:[0,1] op_sel_hi:[1,1]
	v_pk_mul_f32 v[230:231], v[32:33], v[2:3] op_sel:[0,1] op_sel_hi:[1,1]
	v_cvt_pknorm_i16_f32 v8, v228, v229
	s_waitcnt lgkmcnt(0)
	v_max_f32_e32 v13, v13, v235
	v_cvt_pknorm_i16_f32 v9, v230, v231
	v_rcp_f32_e32 v3, v13
	v_cmp_lt_f32_e32 vcc, 0, v13
	s_mov_b64 s[6:7], 0x6400
	v_lshl_add_u64 v[10:11], v[4:5], 0, s[6:7]
	v_cndmask_b32_e32 v3, 0, v3, vcc
	global_store_dwordx4 v[10:11], v[6:9], off sc0 sc1
	v_pk_mul_f32 v[224:225], v[34:35], v[2:3] op_sel:[0,1] op_sel_hi:[1,1]
	v_pk_mul_f32 v[226:227], v[36:37], v[2:3] op_sel:[0,1] op_sel_hi:[1,1]
	v_cvt_pknorm_i16_f32 v6, v224, v225
	v_cvt_pknorm_i16_f32 v7, v226, v227
	v_pk_mul_f32 v[228:229], v[38:39], v[2:3] op_sel:[0,1] op_sel_hi:[1,1]
	v_pk_mul_f32 v[230:231], v[40:41], v[2:3] op_sel:[0,1] op_sel_hi:[1,1]
	v_cvt_pknorm_i16_f32 v8, v228, v229
	s_mov_b64 s[6:7], 0x6600
	v_cvt_pknorm_i16_f32 v9, v230, v231
	v_lshl_add_u64 v[10:11], v[4:5], 0, s[6:7]
	global_store_dwordx4 v[10:11], v[6:9], off sc0 sc1
	s_nop 1
	v_pk_mul_f32 v[6:7], v[12:13], s[4:5] op_sel_hi:[1,0]
	global_store_dwordx2 v0, v[6:7], s[2:3] offset:200
	v_accvgpr_read_b32 v3, a252
	v_accvgpr_read_b32 v6, a236
	v_accvgpr_read_b32 v7, a220
	v_max3_f32 v8, |v3|, |v6|, |v7|
	v_accvgpr_read_b32 v9, a204
	v_accvgpr_read_b32 v14, a188
	v_max3_f32 v8, |v8|, |v9|, |v14|
	v_accvgpr_read_b32 v15, a172
	v_accvgpr_read_b32 v16, a156
	v_max3_f32 v8, |v8|, |v15|, |v16|
	v_accvgpr_read_b32 v10, a108
	v_accvgpr_read_b32 v17, a108
	v_max3_f32 v8, |v8|, |v17|, |v10|
	v_accvgpr_read_b32 v18, a253
	v_accvgpr_read_b32 v19, a237
	v_accvgpr_read_b32 v20, a221
	v_max3_f32 v10, |v18|, |v19|, |v20|
	v_accvgpr_read_b32 v21, a205
	v_accvgpr_read_b32 v22, a189
	v_max3_f32 v10, |v10|, |v21|, |v22|
	v_accvgpr_read_b32 v23, a173
	v_accvgpr_read_b32 v24, a157
	v_max3_f32 v10, |v10|, |v23|, |v24|
	v_accvgpr_read_b32 v25, a109
	v_max3_f32 v11, |v10|, |v25|, |v25|
	v_accvgpr_read_b32 v26, a254
	v_accvgpr_read_b32 v27, a238
	v_accvgpr_read_b32 v28, a222
	v_max3_f32 v10, |v26|, |v27|, |v28|
	v_accvgpr_read_b32 v29, a206
	v_accvgpr_read_b32 v30, a190
	v_max3_f32 v10, |v10|, |v29|, |v30|
	v_accvgpr_read_b32 v31, a174
	v_accvgpr_read_b32 v32, a158
	v_max3_f32 v10, |v10|, |v31|, |v32|
	v_accvgpr_read_b32 v33, a110
	v_max3_f32 v12, |v10|, |v33|, |v33|
	v_accvgpr_read_b32 v34, a255
	v_accvgpr_read_b32 v35, a239
	v_accvgpr_read_b32 v36, a223
	v_max3_f32 v10, |v34|, |v35|, |v36|
	v_accvgpr_read_b32 v37, a207
	v_accvgpr_read_b32 v38, a191
	v_max3_f32 v10, |v10|, |v37|, |v38|
	v_accvgpr_read_b32 v39, a175
	v_accvgpr_read_b32 v40, a159
	v_max3_f32 v10, |v10|, |v39|, |v40|
	v_accvgpr_read_b32 v41, a111
	v_max3_f32 v13, |v10|, |v41|, |v41|
	s_mov_b64 s[6:7], 0x7000
	s_nop 1
	v_max_f32_dpp v8, v8, v8 quad_perm:[1,0,3,2] row_mask:0xf bank_mask:0xf
	v_max_f32_dpp v11, v11, v11 quad_perm:[1,0,3,2] row_mask:0xf bank_mask:0xf
	v_max_f32_dpp v12, v12, v12 quad_perm:[1,0,3,2] row_mask:0xf bank_mask:0xf
	v_max_f32_dpp v13, v13, v13 quad_perm:[1,0,3,2] row_mask:0xf bank_mask:0xf
	v_max_f32_dpp v8, v8, v8 quad_perm:[2,3,0,1] row_mask:0xf bank_mask:0xf
	v_max_f32_dpp v11, v11, v11 quad_perm:[2,3,0,1] row_mask:0xf bank_mask:0xf
	v_max_f32_dpp v12, v12, v12 quad_perm:[2,3,0,1] row_mask:0xf bank_mask:0xf
	v_max_f32_dpp v13, v13, v13 quad_perm:[2,3,0,1] row_mask:0xf bank_mask:0xf
	v_max_f32_dpp v8, v8, v8 row_half_mirror row_mask:0xf bank_mask:0xf
	v_max_f32_dpp v11, v11, v11 row_half_mirror row_mask:0xf bank_mask:0xf
	v_max_f32_dpp v12, v12, v12 row_half_mirror row_mask:0xf bank_mask:0xf
	v_max_f32_dpp v13, v13, v13 row_half_mirror row_mask:0xf bank_mask:0xf
	v_max_f32_dpp v8, v8, v8 row_mirror row_mask:0xf bank_mask:0xf
	v_max_f32_dpp v11, v11, v11 row_mirror row_mask:0xf bank_mask:0xf
	v_max_f32_dpp v12, v12, v12 row_mirror row_mask:0xf bank_mask:0xf
	v_max_f32_dpp v13, v13, v13 row_mirror row_mask:0xf bank_mask:0xf
	s_nop 0
	ds_swizzle_b32 v232, v8 offset:swizzle(SWAP,16)
	ds_swizzle_b32 v233, v11 offset:swizzle(SWAP,16)
	ds_swizzle_b32 v234, v12 offset:swizzle(SWAP,16)
	ds_swizzle_b32 v235, v13 offset:swizzle(SWAP,16)
	s_waitcnt lgkmcnt(0)
	v_max_f32_e32 v10, v8, v232
	v_rcp_f32_e32 v8, v10
	v_cmp_lt_f32_e32 vcc, 0, v10
	s_waitcnt lgkmcnt(0)
	v_max_f32_e32 v11, v11, v233
	s_waitcnt lgkmcnt(0)
	v_max_f32_e32 v12, v12, v234
	v_cndmask_b32_e32 v42, 0, v8, vcc
	v_mul_f32_e32 v3, v42, v3
	v_mul_f32_e32 v6, v42, v6
	v_cvt_pknorm_i16_f32 v6, v3, v6
	v_mul_f32_e32 v3, v42, v7
	v_mul_f32_e32 v7, v42, v9
	v_cvt_pknorm_i16_f32 v7, v3, v7
	v_pk_mul_f32 v[224:225], v[14:15], v[42:43] op_sel_hi:[1,0]
	v_pk_mul_f32 v[226:227], v[16:17], v[42:43] op_sel_hi:[1,0]
	v_cvt_pknorm_i16_f32 v8, v224, v225
	v_cvt_pknorm_i16_f32 v9, v226, v227
	v_rcp_f32_e32 v3, v11
	v_cmp_lt_f32_e32 vcc, 0, v11
	v_lshl_add_u64 v[14:15], v[4:5], 0, s[6:7]
	global_store_dwordx4 v[14:15], v[6:9], off sc0 sc1
	s_mov_b64 s[6:7], 0x7200
	v_cndmask_b32_e32 v3, 0, v3, vcc
	v_pk_mul_f32 v[228:229], v[18:19], v[2:3] op_sel:[0,1] op_sel_hi:[1,1]
	v_pk_mul_f32 v[230:231], v[20:21], v[2:3] op_sel:[0,1] op_sel_hi:[1,1]
	v_cvt_pknorm_i16_f32 v6, v228, v229
	v_cvt_pknorm_i16_f32 v7, v230, v231
	v_pk_mul_f32 v[224:225], v[22:23], v[2:3] op_sel:[0,1] op_sel_hi:[1,1]
	v_pk_mul_f32 v[226:227], v[24:25], v[2:3] op_sel:[0,1] op_sel_hi:[1,1]
	v_cvt_pknorm_i16_f32 v8, v224, v225
	v_cvt_pknorm_i16_f32 v9, v226, v227
	v_rcp_f32_e32 v3, v12
	v_cmp_lt_f32_e32 vcc, 0, v12
	v_lshl_add_u64 v[14:15], v[4:5], 0, s[6:7]
	global_store_dwordx4 v[14:15], v[6:9], off sc0 sc1
	s_nop 1
	v_pk_mul_f32 v[6:7], v[10:11], s[4:5] op_sel_hi:[1,0]
	v_cndmask_b32_e32 v3, 0, v3, vcc
	global_store_dwordx2 v0, v[6:7], s[2:3] offset:224
	v_pk_mul_f32 v[228:229], v[26:27], v[2:3] op_sel:[0,1] op_sel_hi:[1,1]
	v_pk_mul_f32 v[230:231], v[28:29], v[2:3] op_sel:[0,1] op_sel_hi:[1,1]
	v_cvt_pknorm_i16_f32 v6, v228, v229
	v_cvt_pknorm_i16_f32 v7, v230, v231
	v_pk_mul_f32 v[224:225], v[30:31], v[2:3] op_sel:[0,1] op_sel_hi:[1,1]
	v_pk_mul_f32 v[226:227], v[32:33], v[2:3] op_sel:[0,1] op_sel_hi:[1,1]
	v_cvt_pknorm_i16_f32 v8, v224, v225
	s_waitcnt lgkmcnt(0)
	v_max_f32_e32 v13, v13, v235
	v_cvt_pknorm_i16_f32 v9, v226, v227
	v_rcp_f32_e32 v3, v13
	v_cmp_lt_f32_e32 vcc, 0, v13
	s_mov_b64 s[6:7], 0x7400
	v_lshl_add_u64 v[10:11], v[4:5], 0, s[6:7]
	v_cndmask_b32_e32 v3, 0, v3, vcc
	global_store_dwordx4 v[10:11], v[6:9], off sc0 sc1
	v_pk_mul_f32 v[228:229], v[34:35], v[2:3] op_sel:[0,1] op_sel_hi:[1,1]
	v_pk_mul_f32 v[230:231], v[36:37], v[2:3] op_sel:[0,1] op_sel_hi:[1,1]
	v_cvt_pknorm_i16_f32 v6, v228, v229
	v_cvt_pknorm_i16_f32 v7, v230, v231
	v_pk_mul_f32 v[224:225], v[38:39], v[2:3] op_sel:[0,1] op_sel_hi:[1,1]
	v_pk_mul_f32 v[226:227], v[40:41], v[2:3] op_sel:[0,1] op_sel_hi:[1,1]
	v_cvt_pknorm_i16_f32 v8, v224, v225
	s_mov_b64 s[6:7], 0x7600
	v_cvt_pknorm_i16_f32 v9, v226, v227
	v_lshl_add_u64 v[4:5], v[4:5], 0, s[6:7]
	global_store_dwordx4 v[4:5], v[6:9], off sc0 sc1
	v_pk_mul_f32 v[4:5], v[12:13], s[4:5] op_sel_hi:[1,0]
	global_store_dwordx2 v0, v[4:5], s[2:3] offset:232
	ds_bpermute_b32 v4, v133, v134
	s_lshl_b64 s[0:1], s[0:1], 2
	s_add_u32 s0, s26, s0
	s_addc_u32 s1, s27, s1
	v_mov_b32_e32 v3, v1
	v_cmp_gt_i32_e32 vcc, 32, v132
	v_lshl_add_u64 v[0:1], s[0:1], 0, v[2:3]
	s_and_saveexec_b64 s[0:1], vcc
	s_cbranch_execz .LBB1_6
	s_waitcnt lgkmcnt(0)
	v_add_f32_e32 v2, v134, v4
	global_store_dword v[0:1], v2, off
